# speedup vs baseline: 1.0087x; 1.0087x over previous
.LBB2_353:
	s_mov_b64 s[80:81], s[78:79]
	s_or_b64 exec, exec, s[10:11]
	v_bfe_i32 v36, v148, 27, 1
	v_lshlrev_b32_e32 v34, 4, v148
	v_lshrrev_b32_e32 v36, 22, v36
	v_add_u32_e32 v36, v34, v36
	v_and_b32_e32 v36, 0xfffffc00, v36
	v_sub_u32_e32 v34, v34, v36
	v_lshrrev_b32_e32 v36, 4, v34
	v_bitop3_b32 v34, v36, v34, 32 bitop3:0x6c
	v_ashrrev_i32_e32 v35, 31, v148
	v_ashrrev_i32_e32 v37, 31, v34
	s_lshl_b64 s[10:11], s[0:1], 22
	v_lshrrev_b32_e32 v35, 26, v35
	v_lshrrev_b32_e32 v37, 26, v37
	s_add_u32 s10, s28, s10
	v_add_u32_e32 v35, v148, v35
	v_add_u32_e32 v37, v34, v37
	s_addc_u32 s11, s29, s11
	s_lshl_b32 s57, s33, 10
	v_ashrrev_i32_e32 v35, 6, v35
	v_lshrrev_b32_e32 v38, 6, v37
	v_and_b32_e32 v37, 0xc0, v37
	s_lshl_b32 s33, s54, 19
	v_lshlrev_b32_e32 v36, 3, v35
	v_lshlrev_b32_e32 v35, 5, v35
	v_sub_u32_e32 v34, v34, v37
	s_add_u32 s92, s10, s33
	v_and_b32_e32 v36, 0x1ffff0, v36
	v_and_b32_e32 v35, 32, v35
	v_ashrrev_i16_sdwa v34, v183, sext(v34) dst_sel:DWORD dst_unused:UNUSED_PAD src0_sel:DWORD src1_sel:BYTE_0
	s_addc_u32 s93, s11, 0
	s_add_i32 s97, s57, 0
	v_add_u32_sdwa v34, v35, sext(v34) dst_sel:DWORD dst_unused:UNUSED_PAD src0_sel:DWORD src1_sel:WORD_0
	v_add_lshl_u32 v35, v38, v36, 11
	s_mov_b64 s[10:11], s[92:93]
	s_add_i32 s84, s97, 0x10000
	v_lshl_add_u32 v162, v34, 1, v35
	s_mov_b32 m0, s84
	v_cmp_eq_u32_e32 vcc, 1, v154
	global_load_lds_dwordx4 v162, s[10:11]
	s_add_u32 s10, s10, 0x20000
	s_addc_u32 s11, s11, 0
	s_add_i32 s94, s97, 0x12000
	s_mov_b32 m0, s94
	s_ashr_i32 s99, s98, 31
	global_load_lds_dwordx4 v162, s[10:11]
	s_lshl_b64 s[10:11], s[98:99], 11
	s_add_u32 s90, s30, s10
	s_addc_u32 s91, s31, s11
	s_mov_b64 s[10:11], s[90:91]
	s_mov_b32 m0, s97
	s_nop 0
	global_load_lds_dwordx4 v162, s[10:11]
	s_add_u32 s10, s10, 0x20000
	s_addc_u32 s11, s11, 0
	s_add_i32 s99, s97, 0x2000
	s_add_u32 s34, s92, 0x40000
	s_mov_b32 m0, s99
	s_addc_u32 s35, s93, 0
	global_load_lds_dwordx4 v162, s[10:11]
	s_mov_b64 s[10:11], s[34:35]
	s_add_i32 s95, s97, 0x14000
	s_mov_b32 m0, s95
	s_nop 0
	global_load_lds_dwordx4 v162, s[10:11]
	s_add_u32 s10, s10, 0x20000
	s_addc_u32 s11, s11, 0
	s_add_i32 s33, s97, 0x16000
	s_mov_b32 m0, s33
	s_nop 0
	global_load_lds_dwordx4 v162, s[10:11]
	s_or_b32 s10, s98, 0x80
	s_ashr_i32 s11, s10, 31
	s_lshl_b64 s[52:53], s[10:11], 11
	s_add_u32 s88, s30, s52
	s_addc_u32 s89, s31, s53
	s_mov_b64 s[52:53], s[88:89]
	s_add_i32 s11, s97, 0x4000
	s_mov_b32 m0, s11
	s_nop 0
	global_load_lds_dwordx4 v162, s[52:53]
	s_add_u32 s52, s52, 0x20000
	s_addc_u32 s53, s53, 0
	s_add_i32 s56, s97, 0x6000
	s_mov_b32 m0, s56
	s_nop 0
	global_load_lds_dwordx4 v162, s[52:53]
	s_and_saveexec_b64 s[52:53], vcc
	s_cbranch_execz .LBB2_355
	s_setprio 1
	s_barrier

.LBB2_356:
	ds_read_b128 v[140:143], v138
	ds_read_b128 v[154:157], v138 offset:1024
	ds_read_b128 v[158:161], v138 offset:2048
	ds_read_b128 v[164:167], v138 offset:3072
	s_lshl_b32 vcc_hi, s57, 7
	s_add_u32 s58, s88, vcc_hi
	s_addc_u32 s59, s89, 0
	s_add_u32 s82, s58, 0x80
	s_addc_u32 s83, s59, 0
	s_add_i32 s59, s97, 0xc000
	v_lshl_add_u64 v[144:145], s[82:83], 0, v[162:163]
	s_add_u32 s82, s82, 0x20000
	s_mov_b32 m0, s59
	s_addc_u32 s83, s83, 0
	s_add_i32 s58, s97, 0xe000
	ds_read_b128 v[168:171], v134
	ds_read_b128 v[172:175], v134 offset:1024
	ds_read_b128 v[176:179], v133
	ds_read_b128 v[184:187], v133 offset:1024
	ds_read_b128 v[188:191], v131
	ds_read_b128 v[192:195], v131 offset:1024
	ds_read_b128 v[196:199], v130
	ds_read_b128 v[200:203], v130 offset:1024
	global_load_lds_dwordx4 v[144:145], off
	s_mov_b32 m0, s58
	v_lshl_add_u64 v[144:145], s[82:83], 0, v[162:163]
	global_load_lds_dwordx4 v[144:145], off
	s_waitcnt lgkmcnt(8)
	s_barrier
	s_waitcnt lgkmcnt(0)
	v_mfma_f32_16x16x32_f16 v[102:105], v[140:143], v[168:171], v[102:105]
	v_mfma_f32_16x16x32_f16 v[98:101], v[158:161], v[168:171], v[98:101]
	v_mfma_f32_16x16x32_f16 v[126:129], v[140:143], v[176:179], v[126:129]
	v_mfma_f32_16x16x32_f16 v[122:125], v[158:161], v[176:179], v[122:125]
	v_mfma_f32_16x16x32_f16 v[118:121], v[140:143], v[188:191], v[118:121]
	v_mfma_f32_16x16x32_f16 v[114:117], v[158:161], v[188:191], v[114:117]
	v_mfma_f32_16x16x32_f16 v[110:113], v[140:143], v[196:199], v[110:113]
	v_mfma_f32_16x16x32_f16 v[106:109], v[158:161], v[196:199], v[106:109]
	v_mfma_f32_16x16x32_f16 v[102:105], v[154:157], v[172:175], v[102:105]
	v_mfma_f32_16x16x32_f16 v[98:101], v[164:167], v[172:175], v[98:101]
	v_mfma_f32_16x16x32_f16 v[126:129], v[154:157], v[184:187], v[126:129]
	v_mfma_f32_16x16x32_f16 v[122:125], v[164:167], v[184:187], v[122:125]
	v_mfma_f32_16x16x32_f16 v[118:121], v[154:157], v[192:195], v[118:121]
	v_mfma_f32_16x16x32_f16 v[114:117], v[164:167], v[192:195], v[114:117]
	v_mfma_f32_16x16x32_f16 v[110:113], v[154:157], v[200:203], v[110:113]
	v_mfma_f32_16x16x32_f16 v[106:109], v[164:167], v[200:203], v[106:109]
	s_barrier
	s_add_i32 vcc_lo, s57, 2
	s_lshl_b32 s78, vcc_lo, 7
	s_add_u32 s82, s92, s78
	s_addc_u32 s83, s93, 0
	s_mov_b32 m0, s84
	v_lshl_add_u64 v[144:145], s[82:83], 0, v[162:163]
	s_add_u32 s82, s82, 0x20000
	s_addc_u32 s83, s83, 0
	ds_read_b128 v[204:207], v137
	ds_read_b128 v[208:211], v137 offset:1024
	ds_read_b128 v[212:215], v137 offset:2048
	ds_read_b128 v[216:219], v137 offset:3072
	global_load_lds_dwordx4 v[144:145], off
	s_mov_b32 m0, s94
	v_lshl_add_u64 v[144:145], s[82:83], 0, v[162:163]
	global_load_lds_dwordx4 v[144:145], off
	s_barrier
	s_waitcnt lgkmcnt(0)
	v_mfma_f32_16x16x32_f16 v[94:97], v[204:207], v[168:171], v[94:97]
	v_mfma_f32_16x16x32_f16 v[90:93], v[212:215], v[168:171], v[90:93]
	v_mfma_f32_16x16x32_f16 v[86:89], v[204:207], v[176:179], v[86:89]
	v_mfma_f32_16x16x32_f16 v[82:85], v[212:215], v[176:179], v[82:85]
	v_mfma_f32_16x16x32_f16 v[78:81], v[204:207], v[188:191], v[78:81]
	v_mfma_f32_16x16x32_f16 v[74:77], v[212:215], v[188:191], v[74:77]
	v_mfma_f32_16x16x32_f16 v[70:73], v[204:207], v[196:199], v[70:73]
	v_mfma_f32_16x16x32_f16 v[66:69], v[212:215], v[196:199], v[66:69]
	v_mfma_f32_16x16x32_f16 v[94:97], v[208:211], v[172:175], v[94:97]
	v_mfma_f32_16x16x32_f16 v[90:93], v[216:219], v[172:175], v[90:93]
	v_mfma_f32_16x16x32_f16 v[86:89], v[208:211], v[184:187], v[86:89]
	v_mfma_f32_16x16x32_f16 v[82:85], v[216:219], v[184:187], v[82:85]
	v_mfma_f32_16x16x32_f16 v[78:81], v[208:211], v[192:195], v[78:81]
	v_mfma_f32_16x16x32_f16 v[74:77], v[216:219], v[192:195], v[74:77]
	v_mfma_f32_16x16x32_f16 v[70:73], v[208:211], v[200:203], v[70:73]
	v_mfma_f32_16x16x32_f16 v[66:69], v[216:219], v[200:203], v[66:69]
	s_add_u32 s82, s90, s78
	s_addc_u32 s83, s91, 0
	s_mov_b32 m0, s97
	v_lshl_add_u64 v[144:145], s[82:83], 0, v[162:163]
	s_add_u32 s82, s82, 0x20000
	s_addc_u32 s83, s83, 0
	s_barrier
	ds_read_b128 v[168:171], v134 offset:16384
	ds_read_b128 v[172:175], v134 offset:17408
	ds_read_b128 v[176:179], v133 offset:16384
	ds_read_b128 v[184:187], v133 offset:17408
	ds_read_b128 v[188:191], v131 offset:16384
	ds_read_b128 v[192:195], v131 offset:17408
	ds_read_b128 v[196:199], v130 offset:16384
	ds_read_b128 v[200:203], v130 offset:17408
	global_load_lds_dwordx4 v[144:145], off
	s_mov_b32 m0, s99
	v_lshl_add_u64 v[144:145], s[82:83], 0, v[162:163]
	global_load_lds_dwordx4 v[144:145], off
	s_barrier
	s_waitcnt lgkmcnt(0)
	v_mfma_f32_16x16x32_f16 v[62:65], v[140:143], v[168:171], v[62:65]
	v_mfma_f32_16x16x32_f16 v[58:61], v[158:161], v[168:171], v[58:61]
	v_mfma_f32_16x16x32_f16 v[54:57], v[140:143], v[176:179], v[54:57]
	v_mfma_f32_16x16x32_f16 v[50:53], v[158:161], v[176:179], v[50:53]
	v_mfma_f32_16x16x32_f16 v[46:49], v[140:143], v[188:191], v[46:49]
	v_mfma_f32_16x16x32_f16 v[42:45], v[158:161], v[188:191], v[42:45]
	v_mfma_f32_16x16x32_f16 v[38:41], v[140:143], v[196:199], v[38:41]
	v_mfma_f32_16x16x32_f16 v[30:33], v[158:161], v[196:199], v[30:33]
	v_mfma_f32_16x16x32_f16 v[62:65], v[154:157], v[172:175], v[62:65]
	v_mfma_f32_16x16x32_f16 v[58:61], v[164:167], v[172:175], v[58:61]
	v_mfma_f32_16x16x32_f16 v[54:57], v[154:157], v[184:187], v[54:57]
	v_mfma_f32_16x16x32_f16 v[50:53], v[164:167], v[184:187], v[50:53]
	v_mfma_f32_16x16x32_f16 v[46:49], v[154:157], v[192:195], v[46:49]
	v_mfma_f32_16x16x32_f16 v[42:45], v[164:167], v[192:195], v[42:45]
	v_mfma_f32_16x16x32_f16 v[38:41], v[154:157], v[200:203], v[38:41]
	v_mfma_f32_16x16x32_f16 v[30:33], v[164:167], v[200:203], v[30:33]
	s_barrier
	s_add_u32 s82, s34, s78
	s_addc_u32 s83, s35, 0
	s_mov_b32 m0, s95
	v_lshl_add_u64 v[140:141], s[82:83], 0, v[162:163]
	s_add_u32 s82, s82, 0x20000
	s_addc_u32 s83, s83, 0
	global_load_lds_dwordx4 v[140:141], off
	s_mov_b32 m0, s33
	v_lshl_add_u64 v[140:141], s[82:83], 0, v[162:163]
	global_load_lds_dwordx4 v[140:141], off
	s_waitcnt vmcnt(6)
	s_barrier
	v_mfma_f32_16x16x32_f16 v[34:37], v[204:207], v[168:171], v[34:37]
	v_mfma_f32_16x16x32_f16 v[26:29], v[212:215], v[168:171], v[26:29]
	v_mfma_f32_16x16x32_f16 v[22:25], v[204:207], v[176:179], v[22:25]
	v_mfma_f32_16x16x32_f16 v[18:21], v[212:215], v[176:179], v[18:21]
	v_mfma_f32_16x16x32_f16 v[14:17], v[204:207], v[188:191], v[14:17]
	v_mfma_f32_16x16x32_f16 v[10:13], v[212:215], v[188:191], v[10:13]
	v_mfma_f32_16x16x32_f16 v[6:9], v[204:207], v[196:199], v[6:9]
	v_mfma_f32_16x16x32_f16 v[2:5], v[212:215], v[196:199], v[2:5]
	v_mfma_f32_16x16x32_f16 v[34:37], v[208:211], v[172:175], v[34:37]
	v_mfma_f32_16x16x32_f16 v[26:29], v[216:219], v[172:175], v[26:29]
	v_mfma_f32_16x16x32_f16 v[22:25], v[208:211], v[184:187], v[22:25]
	v_mfma_f32_16x16x32_f16 v[18:21], v[216:219], v[184:187], v[18:21]
	v_mfma_f32_16x16x32_f16 v[14:17], v[208:211], v[192:195], v[14:17]
	v_mfma_f32_16x16x32_f16 v[10:13], v[216:219], v[192:195], v[10:13]
	v_mfma_f32_16x16x32_f16 v[6:9], v[208:211], v[200:203], v[6:9]
	v_mfma_f32_16x16x32_f16 v[2:5], v[216:219], v[200:203], v[2:5]
	s_barrier
	ds_read_b128 v[140:143], v136
	ds_read_b128 v[154:157], v136 offset:1024
	ds_read_b128 v[158:161], v136 offset:2048
	ds_read_b128 v[164:167], v136 offset:3072
	s_add_u32 s82, s88, s78
	s_addc_u32 s83, s89, 0
	s_mov_b32 m0, s11
	v_lshl_add_u64 v[144:145], s[82:83], 0, v[162:163]
	s_add_u32 s82, s82, 0x20000
	s_addc_u32 s83, s83, 0
	ds_read_b128 v[168:171], v134 offset:32768
	ds_read_b128 v[172:175], v134 offset:33792
	ds_read_b128 v[176:179], v133 offset:32768
	ds_read_b128 v[184:187], v133 offset:33792
	ds_read_b128 v[188:191], v131 offset:32768
	ds_read_b128 v[192:195], v131 offset:33792
	ds_read_b128 v[196:199], v130 offset:32768
	ds_read_b128 v[200:203], v130 offset:33792
	global_load_lds_dwordx4 v[144:145], off
	s_mov_b32 m0, s56
	v_lshl_add_u64 v[144:145], s[82:83], 0, v[162:163]
	global_load_lds_dwordx4 v[144:145], off
	s_waitcnt lgkmcnt(8)
	s_barrier
	s_waitcnt lgkmcnt(0)
	v_mfma_f32_16x16x32_f16 v[102:105], v[140:143], v[168:171], v[102:105]
	v_mfma_f32_16x16x32_f16 v[98:101], v[158:161], v[168:171], v[98:101]
	v_mfma_f32_16x16x32_f16 v[126:129], v[140:143], v[176:179], v[126:129]
	v_mfma_f32_16x16x32_f16 v[122:125], v[158:161], v[176:179], v[122:125]
	v_mfma_f32_16x16x32_f16 v[118:121], v[140:143], v[188:191], v[118:121]
	v_mfma_f32_16x16x32_f16 v[114:117], v[158:161], v[188:191], v[114:117]
	v_mfma_f32_16x16x32_f16 v[110:113], v[140:143], v[196:199], v[110:113]
	v_mfma_f32_16x16x32_f16 v[106:109], v[158:161], v[196:199], v[106:109]
	v_mfma_f32_16x16x32_f16 v[102:105], v[154:157], v[172:175], v[102:105]
	v_mfma_f32_16x16x32_f16 v[98:101], v[164:167], v[172:175], v[98:101]
	v_mfma_f32_16x16x32_f16 v[126:129], v[154:157], v[184:187], v[126:129]
	v_mfma_f32_16x16x32_f16 v[122:125], v[164:167], v[184:187], v[122:125]
	v_mfma_f32_16x16x32_f16 v[118:121], v[154:157], v[192:195], v[118:121]
	v_mfma_f32_16x16x32_f16 v[114:117], v[164:167], v[192:195], v[114:117]
	v_mfma_f32_16x16x32_f16 v[110:113], v[154:157], v[200:203], v[110:113]
	v_mfma_f32_16x16x32_f16 v[106:109], v[164:167], v[200:203], v[106:109]
	s_barrier
	s_add_u32 s78, s92, vcc_hi
	s_addc_u32 s79, s93, 0
	s_add_u32 s82, s78, 0x180
	s_addc_u32 s83, s79, 0
	s_add_i32 m0, s97, 0x18000
	v_lshl_add_u64 v[144:145], s[82:83], 0, v[162:163]
	s_add_u32 s82, s82, 0x20000
	s_addc_u32 s83, s83, 0
	ds_read_b128 v[204:207], v135
	ds_read_b128 v[208:211], v135 offset:1024
	ds_read_b128 v[212:215], v135 offset:2048
	ds_read_b128 v[216:219], v135 offset:3072
	global_load_lds_dwordx4 v[144:145], off
	s_add_i32 m0, s97, 0x1a000
	v_lshl_add_u64 v[144:145], s[82:83], 0, v[162:163]
	global_load_lds_dwordx4 v[144:145], off
	s_barrier
	s_waitcnt lgkmcnt(0)
	v_mfma_f32_16x16x32_f16 v[94:97], v[204:207], v[168:171], v[94:97]
	v_mfma_f32_16x16x32_f16 v[90:93], v[212:215], v[168:171], v[90:93]
	v_mfma_f32_16x16x32_f16 v[86:89], v[204:207], v[176:179], v[86:89]
	v_mfma_f32_16x16x32_f16 v[82:85], v[212:215], v[176:179], v[82:85]
	v_mfma_f32_16x16x32_f16 v[78:81], v[204:207], v[188:191], v[78:81]
	v_mfma_f32_16x16x32_f16 v[74:77], v[212:215], v[188:191], v[74:77]
	v_mfma_f32_16x16x32_f16 v[70:73], v[204:207], v[196:199], v[70:73]
	v_mfma_f32_16x16x32_f16 v[66:69], v[212:215], v[196:199], v[66:69]
	v_mfma_f32_16x16x32_f16 v[94:97], v[208:211], v[172:175], v[94:97]
	v_mfma_f32_16x16x32_f16 v[90:93], v[216:219], v[172:175], v[90:93]
	v_mfma_f32_16x16x32_f16 v[86:89], v[208:211], v[184:187], v[86:89]
	v_mfma_f32_16x16x32_f16 v[82:85], v[216:219], v[184:187], v[82:85]
	v_mfma_f32_16x16x32_f16 v[78:81], v[208:211], v[192:195], v[78:81]
	v_mfma_f32_16x16x32_f16 v[74:77], v[216:219], v[192:195], v[74:77]
	v_mfma_f32_16x16x32_f16 v[70:73], v[208:211], v[200:203], v[70:73]
	v_mfma_f32_16x16x32_f16 v[66:69], v[216:219], v[200:203], v[66:69]
	s_add_u32 s78, s90, vcc_hi
	s_addc_u32 s79, s91, 0
	s_add_u32 s82, s78, 0x180
	s_addc_u32 s83, s79, 0
	s_mov_b32 m0, s52
	v_lshl_add_u64 v[144:145], s[82:83], 0, v[162:163]
	s_add_u32 s82, s82, 0x20000
	s_addc_u32 s83, s83, 0
	s_barrier
	ds_read_b128 v[168:171], v134 offset:49152
	ds_read_b128 v[172:175], v134 offset:50176
	ds_read_b128 v[176:179], v133 offset:49152
	ds_read_b128 v[184:187], v133 offset:50176
	ds_read_b128 v[188:191], v131 offset:49152
	ds_read_b128 v[192:195], v131 offset:50176
	ds_read_b128 v[196:199], v130 offset:49152
	ds_read_b128 v[200:203], v130 offset:50176
	global_load_lds_dwordx4 v[144:145], off
	s_mov_b32 m0, s53
	v_lshl_add_u64 v[144:145], s[82:83], 0, v[162:163]
	global_load_lds_dwordx4 v[144:145], off
	s_barrier
	s_waitcnt lgkmcnt(0)
	v_mfma_f32_16x16x32_f16 v[62:65], v[140:143], v[168:171], v[62:65]
	v_mfma_f32_16x16x32_f16 v[58:61], v[158:161], v[168:171], v[58:61]
	v_mfma_f32_16x16x32_f16 v[54:57], v[140:143], v[176:179], v[54:57]
	v_mfma_f32_16x16x32_f16 v[50:53], v[158:161], v[176:179], v[50:53]
	v_mfma_f32_16x16x32_f16 v[46:49], v[140:143], v[188:191], v[46:49]
	v_mfma_f32_16x16x32_f16 v[42:45], v[158:161], v[188:191], v[42:45]
	v_mfma_f32_16x16x32_f16 v[38:41], v[140:143], v[196:199], v[38:41]
	v_mfma_f32_16x16x32_f16 v[30:33], v[158:161], v[196:199], v[30:33]
	v_mfma_f32_16x16x32_f16 v[62:65], v[154:157], v[172:175], v[62:65]
	v_mfma_f32_16x16x32_f16 v[58:61], v[164:167], v[172:175], v[58:61]
	v_mfma_f32_16x16x32_f16 v[54:57], v[154:157], v[184:187], v[54:57]
	v_mfma_f32_16x16x32_f16 v[50:53], v[164:167], v[184:187], v[50:53]
	v_mfma_f32_16x16x32_f16 v[46:49], v[154:157], v[192:195], v[46:49]
	v_mfma_f32_16x16x32_f16 v[42:45], v[164:167], v[192:195], v[42:45]
	v_mfma_f32_16x16x32_f16 v[38:41], v[154:157], v[200:203], v[38:41]
	v_mfma_f32_16x16x32_f16 v[30:33], v[164:167], v[200:203], v[30:33]
	s_barrier
	s_add_u32 s78, s34, vcc_hi
	s_addc_u32 s79, s35, 0
	s_add_u32 s82, s78, 0x180
	s_addc_u32 s83, s79, 0
	s_add_i32 m0, s97, 0x1c000
	v_lshl_add_u64 v[140:141], s[82:83], 0, v[162:163]
	s_add_u32 s82, s82, 0x20000
	s_addc_u32 s83, s83, 0
	global_load_lds_dwordx4 v[140:141], off
	s_add_i32 m0, s97, 0x1e000
	v_lshl_add_u64 v[140:141], s[82:83], 0, v[162:163]
	global_load_lds_dwordx4 v[140:141], off
	s_waitcnt vmcnt(6)
	s_barrier
	v_mfma_f32_16x16x32_f16 v[34:37], v[204:207], v[168:171], v[34:37]
	v_mfma_f32_16x16x32_f16 v[26:29], v[212:215], v[168:171], v[26:29]
	v_mfma_f32_16x16x32_f16 v[22:25], v[204:207], v[176:179], v[22:25]
	v_mfma_f32_16x16x32_f16 v[18:21], v[212:215], v[176:179], v[18:21]
	v_mfma_f32_16x16x32_f16 v[14:17], v[204:207], v[188:191], v[14:17]
	v_mfma_f32_16x16x32_f16 v[10:13], v[212:215], v[188:191], v[10:13]
	v_mfma_f32_16x16x32_f16 v[6:9], v[204:207], v[196:199], v[6:9]
	v_mfma_f32_16x16x32_f16 v[2:5], v[212:215], v[196:199], v[2:5]
	v_mfma_f32_16x16x32_f16 v[34:37], v[208:211], v[172:175], v[34:37]
	v_mfma_f32_16x16x32_f16 v[26:29], v[216:219], v[172:175], v[26:29]
	v_mfma_f32_16x16x32_f16 v[22:25], v[208:211], v[184:187], v[22:25]
	v_mfma_f32_16x16x32_f16 v[18:21], v[216:219], v[184:187], v[18:21]
	v_mfma_f32_16x16x32_f16 v[14:17], v[208:211], v[192:195], v[14:17]
	v_mfma_f32_16x16x32_f16 v[10:13], v[216:219], v[192:195], v[10:13]
	v_mfma_f32_16x16x32_f16 v[6:9], v[208:211], v[200:203], v[6:9]
	v_mfma_f32_16x16x32_f16 v[2:5], v[216:219], v[200:203], v[2:5]
	s_cmp_lt_u32 s57, 12
	s_mov_b32 s57, vcc_lo
	s_barrier
	s_cbranch_scc1 .LBB2_356
	s_add_u32 s34, s88, 0x780
	s_addc_u32 s35, s89, 0
	ds_read_b128 v[140:143], v138
	ds_read_b128 v[154:157], v138 offset:1024
	ds_read_b128 v[158:161], v138 offset:2048
	ds_read_b128 v[164:167], v138 offset:3072
	ds_read_b128 v[168:171], v134
	ds_read_b128 v[172:175], v134 offset:1024
	ds_read_b128 v[176:179], v133
	ds_read_b128 v[184:187], v133 offset:1024
	ds_read_b128 v[188:191], v131
	ds_read_b128 v[192:195], v131 offset:1024
	ds_read_b128 v[196:199], v130
	ds_read_b128 v[200:203], v130 offset:1024
	v_lshl_add_u64 v[138:139], s[34:35], 0, v[162:163]
	s_add_u32 s34, s34, 0x20000
	s_mov_b32 m0, s59
	s_addc_u32 s35, s35, 0
	global_load_lds_dwordx4 v[138:139], off
	s_mov_b32 m0, s58
	v_lshl_add_u64 v[138:139], s[34:35], 0, v[162:163]
	global_load_lds_dwordx4 v[138:139], off
	s_barrier
	s_waitcnt lgkmcnt(0)
	v_mfma_f32_16x16x32_f16 v[102:105], v[140:143], v[168:171], v[102:105]
	v_mfma_f32_16x16x32_f16 v[98:101], v[158:161], v[168:171], v[98:101]
	v_mfma_f32_16x16x32_f16 v[126:129], v[140:143], v[176:179], v[126:129]
	v_mfma_f32_16x16x32_f16 v[122:125], v[158:161], v[176:179], v[122:125]
	v_mfma_f32_16x16x32_f16 v[118:121], v[140:143], v[188:191], v[118:121]
	v_mfma_f32_16x16x32_f16 v[114:117], v[158:161], v[188:191], v[114:117]
	v_mfma_f32_16x16x32_f16 v[110:113], v[140:143], v[196:199], v[110:113]
	v_mfma_f32_16x16x32_f16 v[106:109], v[158:161], v[196:199], v[106:109]
	v_mfma_f32_16x16x32_f16 v[102:105], v[154:157], v[172:175], v[102:105]
	v_mfma_f32_16x16x32_f16 v[98:101], v[164:167], v[172:175], v[98:101]
	v_mfma_f32_16x16x32_f16 v[126:129], v[154:157], v[184:187], v[126:129]
	v_mfma_f32_16x16x32_f16 v[122:125], v[164:167], v[184:187], v[122:125]
	v_mfma_f32_16x16x32_f16 v[118:121], v[154:157], v[192:195], v[118:121]
	v_mfma_f32_16x16x32_f16 v[114:117], v[164:167], v[192:195], v[114:117]
	v_mfma_f32_16x16x32_f16 v[110:113], v[154:157], v[200:203], v[110:113]
	v_mfma_f32_16x16x32_f16 v[106:109], v[164:167], v[200:203], v[106:109]
	s_barrier
	ds_read_b128 v[204:207], v137
	ds_read_b128 v[208:211], v137 offset:1024
	ds_read_b128 v[212:215], v137 offset:2048
	ds_read_b128 v[216:219], v137 offset:3072
	s_barrier
	s_waitcnt lgkmcnt(0)
	v_mfma_f32_16x16x32_f16 v[94:97], v[204:207], v[168:171], v[94:97]
	v_mfma_f32_16x16x32_f16 v[94:97], v[208:211], v[172:175], v[94:97]
	v_mfma_f32_16x16x32_f16 v[90:93], v[212:215], v[168:171], v[90:93]
	v_mfma_f32_16x16x32_f16 v[86:89], v[204:207], v[176:179], v[86:89]
	v_mfma_f32_16x16x32_f16 v[82:85], v[212:215], v[176:179], v[82:85]
	v_mfma_f32_16x16x32_f16 v[78:81], v[204:207], v[188:191], v[78:81]
	v_mfma_f32_16x16x32_f16 v[74:77], v[212:215], v[188:191], v[74:77]
	v_mfma_f32_16x16x32_f16 v[70:73], v[204:207], v[196:199], v[70:73]
	v_mfma_f32_16x16x32_f16 v[66:69], v[212:215], v[196:199], v[66:69]
	v_mfma_f32_16x16x32_f16 v[168:171], v[216:219], v[172:175], v[90:93]
	v_mfma_f32_16x16x32_f16 v[172:175], v[208:211], v[184:187], v[86:89]
	v_mfma_f32_16x16x32_f16 v[176:179], v[216:219], v[184:187], v[82:85]
	v_mfma_f32_16x16x32_f16 v[184:187], v[208:211], v[192:195], v[78:81]
	v_mfma_f32_16x16x32_f16 v[188:191], v[216:219], v[192:195], v[74:77]
	v_mfma_f32_16x16x32_f16 v[192:195], v[208:211], v[200:203], v[70:73]
	v_mfma_f32_16x16x32_f16 v[196:199], v[216:219], v[200:203], v[66:69]
	s_barrier
	s_nop 0
	ds_read_b128 v[66:69], v134 offset:16384
	ds_read_b128 v[70:73], v134 offset:17408
	ds_read_b128 v[74:77], v133 offset:16384
	ds_read_b128 v[78:81], v133 offset:17408
	ds_read_b128 v[82:85], v131 offset:16384
	ds_read_b128 v[86:89], v131 offset:17408
	ds_read_b128 v[90:93], v130 offset:16384
	ds_read_b128 v[200:203], v130 offset:17408
	s_waitcnt vmcnt(4)
	s_barrier
	s_waitcnt lgkmcnt(0)
	v_mfma_f32_16x16x32_f16 v[62:65], v[140:143], v[66:69], v[62:65]
	v_mfma_f32_16x16x32_f16 v[58:61], v[158:161], v[66:69], v[58:61]
	v_mfma_f32_16x16x32_f16 v[54:57], v[140:143], v[74:77], v[54:57]
	v_mfma_f32_16x16x32_f16 v[50:53], v[158:161], v[74:77], v[50:53]
	v_mfma_f32_16x16x32_f16 v[46:49], v[140:143], v[82:85], v[46:49]
	v_mfma_f32_16x16x32_f16 v[42:45], v[158:161], v[82:85], v[42:45]
	v_mfma_f32_16x16x32_f16 v[38:41], v[140:143], v[90:93], v[38:41]
	v_mfma_f32_16x16x32_f16 v[62:65], v[154:157], v[70:73], v[62:65]
	v_mfma_f32_16x16x32_f16 v[58:61], v[164:167], v[70:73], v[58:61]
	v_mfma_f32_16x16x32_f16 v[54:57], v[154:157], v[78:81], v[54:57]
	v_mfma_f32_16x16x32_f16 v[50:53], v[164:167], v[78:81], v[50:53]
	v_mfma_f32_16x16x32_f16 v[46:49], v[154:157], v[86:89], v[46:49]
	v_mfma_f32_16x16x32_f16 v[42:45], v[164:167], v[86:89], v[42:45]
	v_mfma_f32_16x16x32_f16 v[38:41], v[154:157], v[200:203], v[38:41]
	v_mfma_f32_16x16x32_f16 v[30:33], v[158:161], v[90:93], v[30:33]
	v_mfma_f32_16x16x32_f16 v[138:141], v[164:167], v[200:203], v[30:33]
	v_mfma_f32_16x16x32_f16 v[30:33], v[204:207], v[66:69], v[34:37]
	v_mfma_f32_16x16x32_f16 v[34:37], v[208:211], v[70:73], v[30:33]
	v_mfma_f32_16x16x32_f16 v[26:29], v[212:215], v[66:69], v[26:29]
	v_mfma_f32_16x16x32_f16 v[22:25], v[204:207], v[74:77], v[22:25]
	v_mfma_f32_16x16x32_f16 v[18:21], v[212:215], v[74:77], v[18:21]
	v_mfma_f32_16x16x32_f16 v[14:17], v[204:207], v[82:85], v[14:17]
	v_mfma_f32_16x16x32_f16 v[10:13], v[212:215], v[82:85], v[10:13]
	v_mfma_f32_16x16x32_f16 v[6:9], v[204:207], v[90:93], v[6:9]
	v_mfma_f32_16x16x32_f16 v[2:5], v[212:215], v[90:93], v[2:5]
	v_mfma_f32_16x16x32_f16 v[142:145], v[216:219], v[70:73], v[26:29]
	v_mfma_f32_16x16x32_f16 v[154:157], v[208:211], v[78:81], v[22:25]
	v_mfma_f32_16x16x32_f16 v[158:161], v[216:219], v[78:81], v[18:21]
	v_mfma_f32_16x16x32_f16 v[164:167], v[208:211], v[86:89], v[14:17]
	v_mfma_f32_16x16x32_f16 v[220:223], v[216:219], v[86:89], v[10:13]
	v_mfma_f32_16x16x32_f16 v[204:207], v[208:211], v[200:203], v[6:9]
	v_mfma_f32_16x16x32_f16 v[200:203], v[216:219], v[200:203], v[2:5]
	s_barrier
	s_nop 0
	ds_read_b128 v[2:5], v136
	ds_read_b128 v[6:9], v136 offset:1024
	ds_read_b128 v[208:211], v136 offset:2048
	ds_read_b128 v[212:215], v136 offset:3072
	ds_read_b128 v[10:13], v134 offset:32768
	ds_read_b128 v[14:17], v134 offset:33792
	ds_read_b128 v[18:21], v133 offset:32768
	ds_read_b128 v[22:25], v133 offset:33792
	ds_read_b128 v[26:29], v131 offset:32768
	ds_read_b128 v[30:33], v131 offset:33792
	ds_read_b128 v[216:219], v130 offset:32768
	ds_read_b128 v[224:227], v130 offset:33792
	s_waitcnt vmcnt(2)
	s_barrier
	s_waitcnt lgkmcnt(0)
	v_mfma_f32_16x16x32_f16 v[66:69], v[2:5], v[10:13], v[102:105]
	v_mfma_f32_16x16x32_f16 v[90:93], v[6:9], v[14:17], v[66:69]
	v_mfma_f32_16x16x32_f16 v[66:69], v[208:211], v[10:13], v[98:101]
	v_mfma_f32_16x16x32_f16 v[98:101], v[212:215], v[14:17], v[66:69]
	v_mfma_f32_16x16x32_f16 v[66:69], v[2:5], v[18:21], v[126:129]
	v_mfma_f32_16x16x32_f16 v[82:85], v[6:9], v[22:25], v[66:69]
	v_mfma_f32_16x16x32_f16 v[66:69], v[208:211], v[18:21], v[122:125]
	v_mfma_f32_16x16x32_f16 v[86:89], v[212:215], v[22:25], v[66:69]
	v_mfma_f32_16x16x32_f16 v[66:69], v[2:5], v[26:29], v[118:121]
	v_mfma_f32_16x16x32_f16 v[74:77], v[6:9], v[30:33], v[66:69]
	v_mfma_f32_16x16x32_f16 v[66:69], v[208:211], v[26:29], v[114:117]
	v_mfma_f32_16x16x32_f16 v[78:81], v[212:215], v[30:33], v[66:69]
	v_mfma_f32_16x16x32_f16 v[66:69], v[2:5], v[216:219], v[110:113]
	v_mfma_f32_16x16x32_f16 v[70:73], v[208:211], v[216:219], v[106:109]
	v_mfma_f32_16x16x32_f16 v[66:69], v[6:9], v[224:227], v[66:69]
	v_mfma_f32_16x16x32_f16 v[70:73], v[212:215], v[224:227], v[70:73]
	s_barrier
	ds_read_b128 v[228:231], v135
	ds_read_b128 v[232:235], v135 offset:1024
	ds_read_b128 v[236:239], v135 offset:2048
	ds_read_b128 v[240:243], v135 offset:3072
	s_waitcnt vmcnt(0)
	s_barrier
	s_waitcnt lgkmcnt(0)
	v_mfma_f32_16x16x32_f16 v[94:97], v[228:231], v[10:13], v[94:97]
	v_mfma_f32_16x16x32_f16 v[10:13], v[236:239], v[10:13], v[168:171]
	v_mfma_f32_16x16x32_f16 v[126:129], v[240:243], v[14:17], v[10:13]
	v_mfma_f32_16x16x32_f16 v[10:13], v[228:231], v[18:21], v[172:175]
	v_mfma_f32_16x16x32_f16 v[114:117], v[232:235], v[22:25], v[10:13]
	v_mfma_f32_16x16x32_f16 v[10:13], v[236:239], v[18:21], v[176:179]
	v_mfma_f32_16x16x32_f16 v[118:121], v[240:243], v[22:25], v[10:13]
	v_mfma_f32_16x16x32_f16 v[10:13], v[228:231], v[26:29], v[184:187]
	v_mfma_f32_16x16x32_f16 v[106:109], v[232:235], v[30:33], v[10:13]
	v_mfma_f32_16x16x32_f16 v[10:13], v[236:239], v[26:29], v[188:191]
	v_mfma_f32_16x16x32_f16 v[110:113], v[240:243], v[30:33], v[10:13]
	v_mfma_f32_16x16x32_f16 v[10:13], v[228:231], v[216:219], v[192:195]
	v_mfma_f32_16x16x32_f16 v[122:125], v[232:235], v[14:17], v[94:97]
	v_mfma_f32_16x16x32_f16 v[94:97], v[232:235], v[224:227], v[10:13]
	v_mfma_f32_16x16x32_f16 v[10:13], v[236:239], v[216:219], v[196:199]
	v_mfma_f32_16x16x32_f16 v[102:105], v[240:243], v[224:227], v[10:13]
	s_barrier
	ds_read_b128 v[168:171], v134 offset:49152
	ds_read_b128 v[134:137], v134 offset:50176
	ds_read_b128 v[172:175], v133 offset:49152
	ds_read_b128 v[176:179], v133 offset:50176
	ds_read_b128 v[184:187], v131 offset:49152
	ds_read_b128 v[188:191], v131 offset:50176
	ds_read_b128 v[192:195], v130 offset:49152
	ds_read_b128 v[196:199], v130 offset:50176
	s_barrier
	s_waitcnt lgkmcnt(0)
	v_mfma_f32_16x16x32_f16 v[10:13], v[2:5], v[168:171], v[62:65]
	v_mfma_f32_16x16x32_f16 v[26:29], v[6:9], v[134:137], v[10:13]
	v_mfma_f32_16x16x32_f16 v[10:13], v[208:211], v[168:171], v[58:61]
	v_mfma_f32_16x16x32_f16 v[30:33], v[212:215], v[134:137], v[10:13]
	v_mfma_f32_16x16x32_f16 v[10:13], v[2:5], v[172:175], v[54:57]
	v_mfma_f32_16x16x32_f16 v[18:21], v[6:9], v[176:179], v[10:13]
	v_mfma_f32_16x16x32_f16 v[10:13], v[208:211], v[172:175], v[50:53]
	v_mfma_f32_16x16x32_f16 v[22:25], v[212:215], v[176:179], v[10:13]
	v_mfma_f32_16x16x32_f16 v[10:13], v[2:5], v[184:187], v[46:49]
	v_mfma_f32_16x16x32_f16 v[2:5], v[2:5], v[192:195], v[38:41]
	v_mfma_f32_16x16x32_f16 v[10:13], v[6:9], v[188:191], v[10:13]
	v_mfma_f32_16x16x32_f16 v[14:17], v[208:211], v[184:187], v[42:45]
	v_mfma_f32_16x16x32_f16 v[2:5], v[6:9], v[196:199], v[2:5]
	v_mfma_f32_16x16x32_f16 v[6:9], v[208:211], v[192:195], v[138:141]
	v_mfma_f32_16x16x32_f16 v[14:17], v[212:215], v[188:191], v[14:17]
	v_mfma_f32_16x16x32_f16 v[6:9], v[212:215], v[196:199], v[6:9]
	v_mfma_f32_16x16x32_f16 v[34:37], v[228:231], v[168:171], v[34:37]
	v_mfma_f32_16x16x32_f16 v[58:61], v[232:235], v[134:137], v[34:37]
	v_mfma_f32_16x16x32_f16 v[34:37], v[236:239], v[168:171], v[142:145]
	v_mfma_f32_16x16x32_f16 v[62:65], v[240:243], v[134:137], v[34:37]
	v_mfma_f32_16x16x32_f16 v[34:37], v[228:231], v[172:175], v[154:157]
	v_mfma_f32_16x16x32_f16 v[50:53], v[232:235], v[176:179], v[34:37]
	v_mfma_f32_16x16x32_f16 v[34:37], v[236:239], v[172:175], v[158:161]
	v_mfma_f32_16x16x32_f16 v[54:57], v[240:243], v[176:179], v[34:37]
	v_mfma_f32_16x16x32_f16 v[34:37], v[228:231], v[184:187], v[164:167]
	v_mfma_f32_16x16x32_f16 v[42:45], v[232:235], v[188:191], v[34:37]
	v_mfma_f32_16x16x32_f16 v[34:37], v[236:239], v[184:187], v[220:223]
	v_mfma_f32_16x16x32_f16 v[46:49], v[240:243], v[188:191], v[34:37]
	v_mfma_f32_16x16x32_f16 v[34:37], v[228:231], v[192:195], v[204:207]
	v_mfma_f32_16x16x32_f16 v[38:41], v[236:239], v[192:195], v[200:203]
	v_mfma_f32_16x16x32_f16 v[34:37], v[232:235], v[196:199], v[34:37]
	v_mfma_f32_16x16x32_f16 v[38:41], v[240:243], v[196:199], v[38:41]
.Lg2_join:
	s_setprio 0
	s_movk_i32 s11, 0x100
	v_cmp_gt_u32_e32 vcc, s11, v148
	s_barrier
	s_and_saveexec_b64 s[34:35], vcc
	s_cbranch_execz .LBB2_359
	s_barrier

.LBB2_379:
	s_or_b64 exec, exec, s[4:5]
	s_lshl_b64 s[4:5], s[0:1], 23
	v_lshlrev_b32_e32 v5, 6, v5
	s_add_u32 s4, s26, s4
	v_sub_u32_e32 v4, v4, v5
	s_addc_u32 s5, s27, s5
	s_lshl_b32 s33, s33, 10
	s_lshl_b32 s10, s54, 20
	v_lshlrev_b32_e32 v3, 5, v3
	v_ashrrev_i16_sdwa v4, v183, sext(v4) dst_sel:DWORD dst_unused:UNUSED_PAD src0_sel:DWORD src1_sel:BYTE_0
	s_add_u32 s4, s4, s10
	v_and_b32_e32 v3, 32, v3
	v_bfe_i32 v4, v4, 0, 16
	s_addc_u32 s5, s5, 0
	s_add_i32 s52, s33, 0
	v_add_lshl_u32 v3, v3, v4, 1
	s_mov_b64 s[10:11], s[4:5]
	s_add_i32 s53, s52, 0x10000
	v_lshl_add_u32 v162, v2, 12, v3
	s_mov_b32 m0, s53
	s_barrier
	global_load_lds_dwordx4 v162, s[10:11]
	s_add_u32 s10, s10, 0x40000
	s_addc_u32 s11, s11, 0
	s_add_i32 s55, s52, 0x12000
	s_mov_b32 m0, s55
	s_add_i32 s86, s52, 0x2000
	global_load_lds_dwordx4 v162, s[10:11]
	s_add_u32 s10, s4, 0x80000
	s_waitcnt vmcnt(2)
	v_lshl_add_u32 v134, v6, 12, v3
	s_mov_b64 s[34:35], s[24:25]
	s_mov_b32 m0, s52
	s_addc_u32 s11, s5, 0
	v_lshl_add_u32 v136, v7, 12, v3
	s_mov_b64 s[56:57], s[10:11]
	global_load_lds_dwordx4 v134, s[34:35]
	s_mov_b32 m0, s86
	s_add_i32 s87, s52, 0x14000
	global_load_lds_dwordx4 v136, s[34:35]
	s_mov_b32 m0, s87
	v_lshl_add_u32 v132, v8, 12, v3
	global_load_lds_dwordx4 v162, s[56:57]
	s_add_u32 s56, s56, 0x40000
	s_addc_u32 s57, s57, 0
	s_add_i32 s88, s52, 0x16000
	s_mov_b32 m0, s88
	s_add_i32 s89, s52, 0x4000
	s_add_i32 s90, s52, 0x6000
	global_load_lds_dwordx4 v162, s[56:57]
	s_mov_b32 m0, s89
	v_lshl_add_u32 v130, v9, 12, v3
	global_load_lds_dwordx4 v132, s[34:35]
	s_mov_b32 m0, s90
	v_ashrrev_i32_e32 v2, 8, v141
	global_load_lds_dwordx4 v130, s[34:35]
	v_cmp_eq_u32_e32 vcc, 1, v2
	s_and_saveexec_b64 s[34:35], vcc
	s_cbranch_execz .LBB2_381
	s_setprio 1
	s_barrier

.LBB2_382:
	ds_read_b128 v[152:155], v151
	ds_read_b128 v[156:159], v151 offset:1024
	ds_read_b128 v[164:167], v151 offset:2048
	ds_read_b128 v[168:171], v151 offset:3072
	s_lshl_b32 s58, s84, 7
	s_add_u32 s59, s24, s58
	s_addc_u32 s91, s25, 0
	s_add_u32 s92, s59, 0x80
	s_addc_u32 s93, s91, 0
	s_add_i32 s56, s52, 0xc000
	s_mov_b32 m0, s56
	v_lshl_add_u64 v[160:161], s[92:93], 0, v[132:133]
	s_add_i32 s33, s52, 0xe000
	ds_read_b128 v[172:175], v147
	ds_read_b128 v[176:179], v147 offset:1024
	ds_read_b128 v[184:187], v146
	ds_read_b128 v[188:191], v146 offset:1024
	ds_read_b128 v[192:195], v145
	ds_read_b128 v[196:199], v145 offset:1024
	ds_read_b128 v[200:203], v144
	ds_read_b128 v[204:207], v144 offset:1024
	global_load_lds_dwordx4 v[160:161], off
	v_lshl_add_u64 v[160:161], s[92:93], 0, v[130:131]
	s_mov_b32 m0, s33
	s_nop 0
	global_load_lds_dwordx4 v[160:161], off
	s_waitcnt lgkmcnt(8)
	s_barrier
	s_waitcnt lgkmcnt(0)
	v_mfma_f32_16x16x32_f16 v[126:129], v[152:155], v[172:175], v[126:129]
	v_mfma_f32_16x16x32_f16 v[122:125], v[164:167], v[172:175], v[122:125]
	v_mfma_f32_16x16x32_f16 v[118:121], v[152:155], v[184:187], v[118:121]
	v_mfma_f32_16x16x32_f16 v[114:117], v[164:167], v[184:187], v[114:117]
	v_mfma_f32_16x16x32_f16 v[110:113], v[152:155], v[192:195], v[110:113]
	v_mfma_f32_16x16x32_f16 v[106:109], v[164:167], v[192:195], v[106:109]
	v_mfma_f32_16x16x32_f16 v[102:105], v[152:155], v[200:203], v[102:105]
	v_mfma_f32_16x16x32_f16 v[98:101], v[164:167], v[200:203], v[98:101]
	v_mfma_f32_16x16x32_f16 v[126:129], v[156:159], v[176:179], v[126:129]
	v_mfma_f32_16x16x32_f16 v[122:125], v[168:171], v[176:179], v[122:125]
	v_mfma_f32_16x16x32_f16 v[118:121], v[156:159], v[188:191], v[118:121]
	v_mfma_f32_16x16x32_f16 v[114:117], v[168:171], v[188:191], v[114:117]
	v_mfma_f32_16x16x32_f16 v[110:113], v[156:159], v[196:199], v[110:113]
	v_mfma_f32_16x16x32_f16 v[106:109], v[168:171], v[196:199], v[106:109]
	v_mfma_f32_16x16x32_f16 v[102:105], v[156:159], v[204:207], v[102:105]
	v_mfma_f32_16x16x32_f16 v[98:101], v[168:171], v[204:207], v[98:101]
	s_barrier
	s_add_i32 s57, s84, 2
	s_lshl_b32 s82, s57, 7
	s_add_u32 s92, s4, s82
	s_addc_u32 s93, s5, 0
	s_mov_b32 m0, s53
	v_lshl_add_u64 v[160:161], s[92:93], 0, v[162:163]
	s_add_u32 s92, s92, 0x40000
	s_addc_u32 s93, s93, 0
	ds_read_b128 v[208:211], v150
	ds_read_b128 v[212:215], v150 offset:1024
	ds_read_b128 v[216:219], v150 offset:2048
	ds_read_b128 v[220:223], v150 offset:3072
	global_load_lds_dwordx4 v[160:161], off
	s_mov_b32 m0, s55
	v_lshl_add_u64 v[160:161], s[92:93], 0, v[162:163]
	global_load_lds_dwordx4 v[160:161], off
	s_barrier
	s_waitcnt lgkmcnt(0)
	v_mfma_f32_16x16x32_f16 v[94:97], v[208:211], v[172:175], v[94:97]
	v_mfma_f32_16x16x32_f16 v[90:93], v[216:219], v[172:175], v[90:93]
	v_mfma_f32_16x16x32_f16 v[86:89], v[208:211], v[184:187], v[86:89]
	v_mfma_f32_16x16x32_f16 v[82:85], v[216:219], v[184:187], v[82:85]
	v_mfma_f32_16x16x32_f16 v[78:81], v[208:211], v[192:195], v[78:81]
	v_mfma_f32_16x16x32_f16 v[74:77], v[216:219], v[192:195], v[74:77]
	v_mfma_f32_16x16x32_f16 v[70:73], v[208:211], v[200:203], v[70:73]
	v_mfma_f32_16x16x32_f16 v[66:69], v[216:219], v[200:203], v[66:69]
	v_mfma_f32_16x16x32_f16 v[94:97], v[212:215], v[176:179], v[94:97]
	v_mfma_f32_16x16x32_f16 v[90:93], v[220:223], v[176:179], v[90:93]
	v_mfma_f32_16x16x32_f16 v[86:89], v[212:215], v[188:191], v[86:89]
	v_mfma_f32_16x16x32_f16 v[82:85], v[220:223], v[188:191], v[82:85]
	v_mfma_f32_16x16x32_f16 v[78:81], v[212:215], v[196:199], v[78:81]
	v_mfma_f32_16x16x32_f16 v[74:77], v[220:223], v[196:199], v[74:77]
	v_mfma_f32_16x16x32_f16 v[70:73], v[212:215], v[204:207], v[70:73]
	v_mfma_f32_16x16x32_f16 v[66:69], v[220:223], v[204:207], v[66:69]
	s_add_u32 s92, s24, s82
	s_addc_u32 s93, s25, 0
	s_mov_b32 m0, s52
	s_barrier
	v_lshl_add_u64 v[160:161], s[92:93], 0, v[134:135]
	ds_read_b128 v[172:175], v147 offset:16384
	ds_read_b128 v[176:179], v147 offset:17408
	ds_read_b128 v[184:187], v146 offset:16384
	ds_read_b128 v[188:191], v146 offset:17408
	ds_read_b128 v[192:195], v145 offset:16384
	ds_read_b128 v[196:199], v145 offset:17408
	ds_read_b128 v[200:203], v144 offset:16384
	ds_read_b128 v[204:207], v144 offset:17408
	global_load_lds_dwordx4 v[160:161], off
	v_lshl_add_u64 v[160:161], s[92:93], 0, v[136:137]
	s_mov_b32 m0, s86
	s_nop 0
	global_load_lds_dwordx4 v[160:161], off
	s_barrier
	s_waitcnt lgkmcnt(0)
	v_mfma_f32_16x16x32_f16 v[62:65], v[152:155], v[172:175], v[62:65]
	v_mfma_f32_16x16x32_f16 v[58:61], v[164:167], v[172:175], v[58:61]
	v_mfma_f32_16x16x32_f16 v[54:57], v[152:155], v[184:187], v[54:57]
	v_mfma_f32_16x16x32_f16 v[50:53], v[164:167], v[184:187], v[50:53]
	v_mfma_f32_16x16x32_f16 v[46:49], v[152:155], v[192:195], v[46:49]
	v_mfma_f32_16x16x32_f16 v[42:45], v[164:167], v[192:195], v[42:45]
	v_mfma_f32_16x16x32_f16 v[38:41], v[152:155], v[200:203], v[38:41]
	v_mfma_f32_16x16x32_f16 v[34:37], v[164:167], v[200:203], v[34:37]
	v_mfma_f32_16x16x32_f16 v[62:65], v[156:159], v[176:179], v[62:65]
	v_mfma_f32_16x16x32_f16 v[58:61], v[168:171], v[176:179], v[58:61]
	v_mfma_f32_16x16x32_f16 v[54:57], v[156:159], v[188:191], v[54:57]
	v_mfma_f32_16x16x32_f16 v[50:53], v[168:171], v[188:191], v[50:53]
	v_mfma_f32_16x16x32_f16 v[46:49], v[156:159], v[196:199], v[46:49]
	v_mfma_f32_16x16x32_f16 v[42:45], v[168:171], v[196:199], v[42:45]
	v_mfma_f32_16x16x32_f16 v[38:41], v[156:159], v[204:207], v[38:41]
	v_mfma_f32_16x16x32_f16 v[34:37], v[168:171], v[204:207], v[34:37]
	s_barrier
	s_add_u32 s94, s10, s82
	s_addc_u32 s95, s11, 0
	s_mov_b32 m0, s87
	v_lshl_add_u64 v[152:153], s[94:95], 0, v[162:163]
	s_add_u32 s94, s94, 0x40000
	s_addc_u32 s95, s95, 0
	global_load_lds_dwordx4 v[152:153], off
	s_mov_b32 m0, s88
	v_lshl_add_u64 v[152:153], s[94:95], 0, v[162:163]
	global_load_lds_dwordx4 v[152:153], off
	s_waitcnt vmcnt(6)
	s_barrier
	v_mfma_f32_16x16x32_f16 v[30:33], v[208:211], v[172:175], v[30:33]
	v_mfma_f32_16x16x32_f16 v[26:29], v[216:219], v[172:175], v[26:29]
	v_mfma_f32_16x16x32_f16 v[22:25], v[208:211], v[184:187], v[22:25]
	v_mfma_f32_16x16x32_f16 v[18:21], v[216:219], v[184:187], v[18:21]
	v_mfma_f32_16x16x32_f16 v[14:17], v[208:211], v[192:195], v[14:17]
	v_mfma_f32_16x16x32_f16 v[10:13], v[216:219], v[192:195], v[10:13]
	v_mfma_f32_16x16x32_f16 v[6:9], v[208:211], v[200:203], v[6:9]
	v_mfma_f32_16x16x32_f16 v[2:5], v[216:219], v[200:203], v[2:5]
	v_mfma_f32_16x16x32_f16 v[30:33], v[212:215], v[176:179], v[30:33]
	v_mfma_f32_16x16x32_f16 v[26:29], v[220:223], v[176:179], v[26:29]
	v_mfma_f32_16x16x32_f16 v[22:25], v[212:215], v[188:191], v[22:25]
	v_mfma_f32_16x16x32_f16 v[18:21], v[220:223], v[188:191], v[18:21]
	v_mfma_f32_16x16x32_f16 v[14:17], v[212:215], v[196:199], v[14:17]
	v_mfma_f32_16x16x32_f16 v[10:13], v[220:223], v[196:199], v[10:13]
	v_mfma_f32_16x16x32_f16 v[6:9], v[212:215], v[204:207], v[6:9]
	v_mfma_f32_16x16x32_f16 v[2:5], v[220:223], v[204:207], v[2:5]
	s_barrier
	ds_read_b128 v[152:155], v149
	ds_read_b128 v[156:159], v149 offset:1024
	ds_read_b128 v[164:167], v149 offset:2048
	ds_read_b128 v[168:171], v149 offset:3072
	s_mov_b32 m0, s89
	v_lshl_add_u64 v[160:161], s[92:93], 0, v[132:133]
	ds_read_b128 v[172:175], v147 offset:32768
	ds_read_b128 v[176:179], v147 offset:33792
	ds_read_b128 v[184:187], v146 offset:32768
	ds_read_b128 v[188:191], v146 offset:33792
	ds_read_b128 v[192:195], v145 offset:32768
	ds_read_b128 v[196:199], v145 offset:33792
	ds_read_b128 v[200:203], v144 offset:32768
	ds_read_b128 v[204:207], v144 offset:33792
	global_load_lds_dwordx4 v[160:161], off
	v_lshl_add_u64 v[160:161], s[92:93], 0, v[130:131]
	s_mov_b32 m0, s90
	s_nop 0
	global_load_lds_dwordx4 v[160:161], off
	s_waitcnt lgkmcnt(8)
	s_barrier
	s_waitcnt lgkmcnt(0)
	v_mfma_f32_16x16x32_f16 v[126:129], v[152:155], v[172:175], v[126:129]
	v_mfma_f32_16x16x32_f16 v[122:125], v[164:167], v[172:175], v[122:125]
	v_mfma_f32_16x16x32_f16 v[118:121], v[152:155], v[184:187], v[118:121]
	v_mfma_f32_16x16x32_f16 v[114:117], v[164:167], v[184:187], v[114:117]
	v_mfma_f32_16x16x32_f16 v[110:113], v[152:155], v[192:195], v[110:113]
	v_mfma_f32_16x16x32_f16 v[106:109], v[164:167], v[192:195], v[106:109]
	v_mfma_f32_16x16x32_f16 v[102:105], v[152:155], v[200:203], v[102:105]
	v_mfma_f32_16x16x32_f16 v[98:101], v[164:167], v[200:203], v[98:101]
	v_mfma_f32_16x16x32_f16 v[126:129], v[156:159], v[176:179], v[126:129]
	v_mfma_f32_16x16x32_f16 v[122:125], v[168:171], v[176:179], v[122:125]
	v_mfma_f32_16x16x32_f16 v[118:121], v[156:159], v[188:191], v[118:121]
	v_mfma_f32_16x16x32_f16 v[114:117], v[168:171], v[188:191], v[114:117]
	v_mfma_f32_16x16x32_f16 v[110:113], v[156:159], v[196:199], v[110:113]
	v_mfma_f32_16x16x32_f16 v[106:109], v[168:171], v[196:199], v[106:109]
	v_mfma_f32_16x16x32_f16 v[102:105], v[156:159], v[204:207], v[102:105]
	v_mfma_f32_16x16x32_f16 v[98:101], v[168:171], v[204:207], v[98:101]
	s_barrier
	s_add_u32 s82, s4, s58
	s_addc_u32 s83, s5, 0
	s_add_u32 s92, s82, 0x180
	s_addc_u32 s93, s83, 0
	s_add_i32 m0, s52, 0x18000
	v_lshl_add_u64 v[160:161], s[92:93], 0, v[162:163]
	s_add_u32 s92, s92, 0x40000
	s_addc_u32 s93, s93, 0
	ds_read_b128 v[208:211], v148
	ds_read_b128 v[212:215], v148 offset:1024
	ds_read_b128 v[216:219], v148 offset:2048
	ds_read_b128 v[220:223], v148 offset:3072
	global_load_lds_dwordx4 v[160:161], off
	s_add_i32 m0, s52, 0x1a000
	v_lshl_add_u64 v[160:161], s[92:93], 0, v[162:163]
	global_load_lds_dwordx4 v[160:161], off
	s_barrier
	s_waitcnt lgkmcnt(0)
	v_mfma_f32_16x16x32_f16 v[94:97], v[208:211], v[172:175], v[94:97]
	v_mfma_f32_16x16x32_f16 v[90:93], v[216:219], v[172:175], v[90:93]
	v_mfma_f32_16x16x32_f16 v[86:89], v[208:211], v[184:187], v[86:89]
	v_mfma_f32_16x16x32_f16 v[82:85], v[216:219], v[184:187], v[82:85]
	v_mfma_f32_16x16x32_f16 v[78:81], v[208:211], v[192:195], v[78:81]
	v_mfma_f32_16x16x32_f16 v[74:77], v[216:219], v[192:195], v[74:77]
	v_mfma_f32_16x16x32_f16 v[70:73], v[208:211], v[200:203], v[70:73]
	v_mfma_f32_16x16x32_f16 v[66:69], v[216:219], v[200:203], v[66:69]
	v_mfma_f32_16x16x32_f16 v[94:97], v[212:215], v[176:179], v[94:97]
	v_mfma_f32_16x16x32_f16 v[90:93], v[220:223], v[176:179], v[90:93]
	v_mfma_f32_16x16x32_f16 v[86:89], v[212:215], v[188:191], v[86:89]
	v_mfma_f32_16x16x32_f16 v[82:85], v[220:223], v[188:191], v[82:85]
	v_mfma_f32_16x16x32_f16 v[78:81], v[212:215], v[196:199], v[78:81]
	v_mfma_f32_16x16x32_f16 v[74:77], v[220:223], v[196:199], v[74:77]
	v_mfma_f32_16x16x32_f16 v[70:73], v[212:215], v[204:207], v[70:73]
	v_mfma_f32_16x16x32_f16 v[66:69], v[220:223], v[204:207], v[66:69]
	s_add_u32 s92, s59, 0x180
	s_addc_u32 s93, s91, 0
	s_mov_b32 m0, s34
	s_barrier
	v_lshl_add_u64 v[160:161], s[92:93], 0, v[134:135]
	ds_read_b128 v[172:175], v147 offset:49152
	ds_read_b128 v[176:179], v147 offset:50176
	ds_read_b128 v[184:187], v146 offset:49152
	ds_read_b128 v[188:191], v146 offset:50176
	ds_read_b128 v[192:195], v145 offset:49152
	ds_read_b128 v[196:199], v145 offset:50176
	ds_read_b128 v[200:203], v144 offset:49152
	ds_read_b128 v[204:207], v144 offset:50176
	global_load_lds_dwordx4 v[160:161], off
	v_lshl_add_u64 v[160:161], s[92:93], 0, v[136:137]
	s_mov_b32 m0, s35
	s_nop 0
	global_load_lds_dwordx4 v[160:161], off
	s_barrier
	s_waitcnt lgkmcnt(0)
	v_mfma_f32_16x16x32_f16 v[62:65], v[152:155], v[172:175], v[62:65]
	v_mfma_f32_16x16x32_f16 v[58:61], v[164:167], v[172:175], v[58:61]
	v_mfma_f32_16x16x32_f16 v[54:57], v[152:155], v[184:187], v[54:57]
	v_mfma_f32_16x16x32_f16 v[50:53], v[164:167], v[184:187], v[50:53]
	v_mfma_f32_16x16x32_f16 v[46:49], v[152:155], v[192:195], v[46:49]
	v_mfma_f32_16x16x32_f16 v[42:45], v[164:167], v[192:195], v[42:45]
	v_mfma_f32_16x16x32_f16 v[38:41], v[152:155], v[200:203], v[38:41]
	v_mfma_f32_16x16x32_f16 v[34:37], v[164:167], v[200:203], v[34:37]
	v_mfma_f32_16x16x32_f16 v[62:65], v[156:159], v[176:179], v[62:65]
	v_mfma_f32_16x16x32_f16 v[58:61], v[168:171], v[176:179], v[58:61]
	v_mfma_f32_16x16x32_f16 v[54:57], v[156:159], v[188:191], v[54:57]
	v_mfma_f32_16x16x32_f16 v[50:53], v[168:171], v[188:191], v[50:53]
	v_mfma_f32_16x16x32_f16 v[46:49], v[156:159], v[196:199], v[46:49]
	v_mfma_f32_16x16x32_f16 v[42:45], v[168:171], v[196:199], v[42:45]
	v_mfma_f32_16x16x32_f16 v[38:41], v[156:159], v[204:207], v[38:41]
	v_mfma_f32_16x16x32_f16 v[34:37], v[168:171], v[204:207], v[34:37]
	s_barrier
	s_add_u32 s58, s10, s58
	s_addc_u32 s59, s11, 0
	s_add_u32 s58, s58, 0x180
	s_addc_u32 s59, s59, 0
	s_add_i32 m0, s52, 0x1c000
	v_lshl_add_u64 v[152:153], s[58:59], 0, v[162:163]
	s_add_u32 s58, s58, 0x40000
	s_addc_u32 s59, s59, 0
	global_load_lds_dwordx4 v[152:153], off
	s_add_i32 m0, s52, 0x1e000
	v_lshl_add_u64 v[152:153], s[58:59], 0, v[162:163]
	global_load_lds_dwordx4 v[152:153], off
	s_waitcnt vmcnt(6)
	s_barrier
	v_mfma_f32_16x16x32_f16 v[30:33], v[208:211], v[172:175], v[30:33]
	v_mfma_f32_16x16x32_f16 v[26:29], v[216:219], v[172:175], v[26:29]
	v_mfma_f32_16x16x32_f16 v[22:25], v[208:211], v[184:187], v[22:25]
	v_mfma_f32_16x16x32_f16 v[18:21], v[216:219], v[184:187], v[18:21]
	v_mfma_f32_16x16x32_f16 v[14:17], v[208:211], v[192:195], v[14:17]
	v_mfma_f32_16x16x32_f16 v[10:13], v[216:219], v[192:195], v[10:13]
	v_mfma_f32_16x16x32_f16 v[6:9], v[208:211], v[200:203], v[6:9]
	v_mfma_f32_16x16x32_f16 v[2:5], v[216:219], v[200:203], v[2:5]
	v_mfma_f32_16x16x32_f16 v[30:33], v[212:215], v[176:179], v[30:33]
	v_mfma_f32_16x16x32_f16 v[26:29], v[220:223], v[176:179], v[26:29]
	v_mfma_f32_16x16x32_f16 v[22:25], v[212:215], v[188:191], v[22:25]
	v_mfma_f32_16x16x32_f16 v[18:21], v[220:223], v[188:191], v[18:21]
	v_mfma_f32_16x16x32_f16 v[14:17], v[212:215], v[196:199], v[14:17]
	v_mfma_f32_16x16x32_f16 v[10:13], v[220:223], v[196:199], v[10:13]
	v_mfma_f32_16x16x32_f16 v[6:9], v[212:215], v[204:207], v[6:9]
	v_mfma_f32_16x16x32_f16 v[2:5], v[220:223], v[204:207], v[2:5]
	s_cmp_lt_u32 s84, 28
	s_mov_b32 s84, s57
	s_barrier
	s_cbranch_scc1 .LBB2_382
	v_readlane_b32 s4, v244, 8
	v_readlane_b32 s5, v244, 9
	s_mov_b32 m0, s56
	ds_read_b128 v[134:137], v151
	ds_read_b128 v[152:155], v151 offset:1024
	ds_read_b128 v[156:159], v151 offset:2048
	ds_read_b128 v[164:167], v151 offset:3072
	ds_read_b128 v[168:171], v147
	ds_read_b128 v[172:175], v147 offset:1024
	ds_read_b128 v[176:179], v146
	ds_read_b128 v[184:187], v146 offset:1024
	ds_read_b128 v[188:191], v145
	ds_read_b128 v[192:195], v145 offset:1024
	ds_read_b128 v[196:199], v144
	ds_read_b128 v[200:203], v144 offset:1024
	v_lshl_add_u64 v[132:133], s[4:5], 0, v[132:133]
	global_load_lds_dwordx4 v[132:133], off
	v_lshl_add_u64 v[130:131], s[4:5], 0, v[130:131]
	s_mov_b32 m0, s33
	s_nop 0
	global_load_lds_dwordx4 v[130:131], off
	s_barrier
	s_waitcnt lgkmcnt(0)
	v_mfma_f32_16x16x32_f16 v[126:129], v[134:137], v[168:171], v[126:129]
	v_mfma_f32_16x16x32_f16 v[122:125], v[156:159], v[168:171], v[122:125]
	v_mfma_f32_16x16x32_f16 v[110:113], v[134:137], v[188:191], v[110:113]
	v_mfma_f32_16x16x32_f16 v[106:109], v[156:159], v[188:191], v[106:109]
	v_mfma_f32_16x16x32_f16 v[126:129], v[152:155], v[172:175], v[126:129]
	v_mfma_f32_16x16x32_f16 v[122:125], v[164:167], v[172:175], v[122:125]
	v_mfma_f32_16x16x32_f16 v[118:121], v[134:137], v[176:179], v[118:121]
	v_mfma_f32_16x16x32_f16 v[114:117], v[156:159], v[176:179], v[114:117]
	v_mfma_f32_16x16x32_f16 v[110:113], v[152:155], v[192:195], v[110:113]
	v_mfma_f32_16x16x32_f16 v[106:109], v[164:167], v[192:195], v[106:109]
	v_mfma_f32_16x16x32_f16 v[102:105], v[134:137], v[196:199], v[102:105]
	v_mfma_f32_16x16x32_f16 v[98:101], v[156:159], v[196:199], v[98:101]
	v_mfma_f32_16x16x32_f16 v[130:133], v[152:155], v[184:187], v[118:121]
	v_mfma_f32_16x16x32_f16 v[204:207], v[164:167], v[184:187], v[114:117]
	v_mfma_f32_16x16x32_f16 v[208:211], v[152:155], v[200:203], v[102:105]
	v_mfma_f32_16x16x32_f16 v[212:215], v[164:167], v[200:203], v[98:101]
	s_barrier
	s_nop 1
	ds_read_b128 v[98:101], v150
	ds_read_b128 v[102:105], v150 offset:1024
	ds_read_b128 v[114:117], v150 offset:2048
	ds_read_b128 v[118:121], v150 offset:3072
	s_barrier
	s_waitcnt lgkmcnt(0)
	v_mfma_f32_16x16x32_f16 v[94:97], v[98:101], v[168:171], v[94:97]
	v_mfma_f32_16x16x32_f16 v[90:93], v[114:117], v[168:171], v[90:93]
	v_mfma_f32_16x16x32_f16 v[78:81], v[98:101], v[188:191], v[78:81]
	v_mfma_f32_16x16x32_f16 v[74:77], v[114:117], v[188:191], v[74:77]
	v_mfma_f32_16x16x32_f16 v[94:97], v[102:105], v[172:175], v[94:97]
	v_mfma_f32_16x16x32_f16 v[90:93], v[118:121], v[172:175], v[90:93]
	v_mfma_f32_16x16x32_f16 v[86:89], v[98:101], v[176:179], v[86:89]
	v_mfma_f32_16x16x32_f16 v[82:85], v[114:117], v[176:179], v[82:85]
	v_mfma_f32_16x16x32_f16 v[78:81], v[102:105], v[192:195], v[78:81]
	v_mfma_f32_16x16x32_f16 v[74:77], v[118:121], v[192:195], v[74:77]
	v_mfma_f32_16x16x32_f16 v[70:73], v[98:101], v[196:199], v[70:73]
	v_mfma_f32_16x16x32_f16 v[66:69], v[114:117], v[196:199], v[66:69]
	v_mfma_f32_16x16x32_f16 v[168:171], v[102:105], v[184:187], v[86:89]
	v_mfma_f32_16x16x32_f16 v[172:175], v[118:121], v[184:187], v[82:85]
	v_mfma_f32_16x16x32_f16 v[176:179], v[102:105], v[200:203], v[70:73]
	v_mfma_f32_16x16x32_f16 v[184:187], v[118:121], v[200:203], v[66:69]
	s_barrier
	s_nop 1
	ds_read_b128 v[66:69], v147 offset:16384
	ds_read_b128 v[70:73], v147 offset:17408
	ds_read_b128 v[82:85], v146 offset:16384
	ds_read_b128 v[86:89], v146 offset:17408
	ds_read_b128 v[188:191], v145 offset:16384
	ds_read_b128 v[192:195], v145 offset:17408
	ds_read_b128 v[196:199], v144 offset:16384
	ds_read_b128 v[200:203], v144 offset:17408
	s_waitcnt vmcnt(4)
	s_barrier
	s_waitcnt lgkmcnt(0)
	v_mfma_f32_16x16x32_f16 v[62:65], v[134:137], v[66:69], v[62:65]
	v_mfma_f32_16x16x32_f16 v[58:61], v[156:159], v[66:69], v[58:61]
	v_mfma_f32_16x16x32_f16 v[46:49], v[134:137], v[188:191], v[46:49]
	v_mfma_f32_16x16x32_f16 v[42:45], v[156:159], v[188:191], v[42:45]
	v_mfma_f32_16x16x32_f16 v[62:65], v[152:155], v[70:73], v[62:65]
	v_mfma_f32_16x16x32_f16 v[58:61], v[164:167], v[70:73], v[58:61]
	v_mfma_f32_16x16x32_f16 v[54:57], v[134:137], v[82:85], v[54:57]
	v_mfma_f32_16x16x32_f16 v[50:53], v[156:159], v[82:85], v[50:53]
	v_mfma_f32_16x16x32_f16 v[46:49], v[152:155], v[192:195], v[46:49]
	v_mfma_f32_16x16x32_f16 v[42:45], v[164:167], v[192:195], v[42:45]
	v_mfma_f32_16x16x32_f16 v[38:41], v[134:137], v[196:199], v[38:41]
	v_mfma_f32_16x16x32_f16 v[34:37], v[156:159], v[196:199], v[34:37]
	v_mfma_f32_16x16x32_f16 v[216:219], v[152:155], v[86:89], v[54:57]
	v_mfma_f32_16x16x32_f16 v[220:223], v[164:167], v[86:89], v[50:53]
	v_mfma_f32_16x16x32_f16 v[134:137], v[152:155], v[200:203], v[38:41]
	v_mfma_f32_16x16x32_f16 v[150:153], v[164:167], v[200:203], v[34:37]
	v_mfma_f32_16x16x32_f16 v[30:33], v[98:101], v[66:69], v[30:33]
	v_mfma_f32_16x16x32_f16 v[26:29], v[114:117], v[66:69], v[26:29]
	v_mfma_f32_16x16x32_f16 v[14:17], v[98:101], v[188:191], v[14:17]
	v_mfma_f32_16x16x32_f16 v[10:13], v[114:117], v[188:191], v[10:13]
	v_mfma_f32_16x16x32_f16 v[30:33], v[102:105], v[70:73], v[30:33]
	v_mfma_f32_16x16x32_f16 v[26:29], v[118:121], v[70:73], v[26:29]
	v_mfma_f32_16x16x32_f16 v[22:25], v[98:101], v[82:85], v[22:25]
	v_mfma_f32_16x16x32_f16 v[18:21], v[114:117], v[82:85], v[18:21]
	v_mfma_f32_16x16x32_f16 v[14:17], v[102:105], v[192:195], v[14:17]
	v_mfma_f32_16x16x32_f16 v[10:13], v[118:121], v[192:195], v[10:13]
	v_mfma_f32_16x16x32_f16 v[6:9], v[98:101], v[196:199], v[6:9]
	v_mfma_f32_16x16x32_f16 v[2:5], v[114:117], v[196:199], v[2:5]
	v_mfma_f32_16x16x32_f16 v[154:157], v[102:105], v[86:89], v[22:25]
	v_mfma_f32_16x16x32_f16 v[158:161], v[118:121], v[86:89], v[18:21]
	v_mfma_f32_16x16x32_f16 v[164:167], v[102:105], v[200:203], v[6:9]
	v_mfma_f32_16x16x32_f16 v[188:191], v[118:121], v[200:203], v[2:5]
	s_barrier
	s_nop 1
	ds_read_b128 v[2:5], v149
	ds_read_b128 v[6:9], v149 offset:1024
	ds_read_b128 v[192:195], v149 offset:2048
	ds_read_b128 v[196:199], v149 offset:3072
	ds_read_b128 v[18:21], v147 offset:32768
	ds_read_b128 v[22:25], v147 offset:33792
	ds_read_b128 v[34:37], v146 offset:32768
	ds_read_b128 v[38:41], v146 offset:33792
	ds_read_b128 v[50:53], v145 offset:32768
	ds_read_b128 v[54:57], v145 offset:33792
	ds_read_b128 v[200:203], v144 offset:32768
	ds_read_b128 v[224:227], v144 offset:33792
	s_waitcnt vmcnt(2)
	s_barrier
	s_waitcnt lgkmcnt(0)
	v_mfma_f32_16x16x32_f16 v[66:69], v[2:5], v[18:21], v[126:129]
	v_mfma_f32_16x16x32_f16 v[118:121], v[6:9], v[22:25], v[66:69]
	v_mfma_f32_16x16x32_f16 v[66:69], v[192:195], v[18:21], v[122:125]
	v_mfma_f32_16x16x32_f16 v[114:117], v[196:199], v[22:25], v[66:69]
	v_mfma_f32_16x16x32_f16 v[66:69], v[2:5], v[34:37], v[130:133]
	v_mfma_f32_16x16x32_f16 v[102:105], v[6:9], v[38:41], v[66:69]
	v_mfma_f32_16x16x32_f16 v[66:69], v[192:195], v[34:37], v[204:207]
	v_mfma_f32_16x16x32_f16 v[98:101], v[196:199], v[38:41], v[66:69]
	v_mfma_f32_16x16x32_f16 v[66:69], v[2:5], v[50:53], v[110:113]
	v_mfma_f32_16x16x32_f16 v[86:89], v[6:9], v[54:57], v[66:69]
	v_mfma_f32_16x16x32_f16 v[66:69], v[192:195], v[50:53], v[106:109]
	v_mfma_f32_16x16x32_f16 v[82:85], v[196:199], v[54:57], v[66:69]
	v_mfma_f32_16x16x32_f16 v[66:69], v[2:5], v[200:203], v[208:211]
	v_mfma_f32_16x16x32_f16 v[70:73], v[6:9], v[224:227], v[66:69]
	v_mfma_f32_16x16x32_f16 v[66:69], v[192:195], v[200:203], v[212:215]
	v_mfma_f32_16x16x32_f16 v[66:69], v[196:199], v[224:227], v[66:69]
	s_barrier
	ds_read_b128 v[130:133], v148
	ds_read_b128 v[204:207], v148 offset:1024
	ds_read_b128 v[208:211], v148 offset:2048
	ds_read_b128 v[212:215], v148 offset:3072
	s_waitcnt vmcnt(0)
	s_barrier
	s_waitcnt lgkmcnt(0)
	v_mfma_f32_16x16x32_f16 v[94:97], v[130:133], v[18:21], v[94:97]
	v_mfma_f32_16x16x32_f16 v[18:21], v[208:211], v[18:21], v[90:93]
	v_mfma_f32_16x16x32_f16 v[122:125], v[212:215], v[22:25], v[18:21]
	v_mfma_f32_16x16x32_f16 v[18:21], v[130:133], v[34:37], v[168:171]
	v_mfma_f32_16x16x32_f16 v[110:113], v[204:207], v[38:41], v[18:21]
	v_mfma_f32_16x16x32_f16 v[18:21], v[208:211], v[34:37], v[172:175]
	v_mfma_f32_16x16x32_f16 v[106:109], v[212:215], v[38:41], v[18:21]
	v_mfma_f32_16x16x32_f16 v[18:21], v[130:133], v[50:53], v[78:81]
	v_mfma_f32_16x16x32_f16 v[126:129], v[204:207], v[22:25], v[94:97]
	v_mfma_f32_16x16x32_f16 v[94:97], v[204:207], v[54:57], v[18:21]
	v_mfma_f32_16x16x32_f16 v[18:21], v[208:211], v[50:53], v[74:77]
	v_mfma_f32_16x16x32_f16 v[90:93], v[212:215], v[54:57], v[18:21]
	v_mfma_f32_16x16x32_f16 v[18:21], v[130:133], v[200:203], v[176:179]
	v_mfma_f32_16x16x32_f16 v[78:81], v[204:207], v[224:227], v[18:21]
	v_mfma_f32_16x16x32_f16 v[18:21], v[208:211], v[200:203], v[184:187]
	v_mfma_f32_16x16x32_f16 v[74:77], v[212:215], v[224:227], v[18:21]
	s_barrier
	ds_read_b128 v[168:171], v147 offset:49152
	ds_read_b128 v[172:175], v147 offset:50176
	ds_read_b128 v[176:179], v146 offset:49152
	ds_read_b128 v[146:149], v146 offset:50176
	ds_read_b128 v[184:187], v145 offset:49152
	ds_read_b128 v[200:203], v145 offset:50176
	ds_read_b128 v[224:227], v144 offset:49152
	ds_read_b128 v[228:231], v144 offset:50176
	s_barrier
	s_waitcnt lgkmcnt(0)
	v_mfma_f32_16x16x32_f16 v[18:21], v[2:5], v[168:171], v[62:65]
	v_mfma_f32_16x16x32_f16 v[54:57], v[6:9], v[172:175], v[18:21]
	v_mfma_f32_16x16x32_f16 v[18:21], v[192:195], v[168:171], v[58:61]
	v_mfma_f32_16x16x32_f16 v[50:53], v[196:199], v[172:175], v[18:21]
	v_mfma_f32_16x16x32_f16 v[18:21], v[2:5], v[176:179], v[216:219]
	v_mfma_f32_16x16x32_f16 v[38:41], v[6:9], v[146:149], v[18:21]
	v_mfma_f32_16x16x32_f16 v[18:21], v[192:195], v[176:179], v[220:223]
	v_mfma_f32_16x16x32_f16 v[34:37], v[196:199], v[146:149], v[18:21]
	v_mfma_f32_16x16x32_f16 v[18:21], v[2:5], v[184:187], v[46:49]
	v_mfma_f32_16x16x32_f16 v[2:5], v[2:5], v[224:227], v[134:137]
	v_mfma_f32_16x16x32_f16 v[22:25], v[6:9], v[200:203], v[18:21]
	v_mfma_f32_16x16x32_f16 v[18:21], v[192:195], v[184:187], v[42:45]
	v_mfma_f32_16x16x32_f16 v[6:9], v[6:9], v[228:231], v[2:5]
	v_mfma_f32_16x16x32_f16 v[2:5], v[192:195], v[224:227], v[150:153]
	v_mfma_f32_16x16x32_f16 v[18:21], v[196:199], v[200:203], v[18:21]
	v_mfma_f32_16x16x32_f16 v[2:5], v[196:199], v[228:231], v[2:5]
	v_mfma_f32_16x16x32_f16 v[26:29], v[208:211], v[168:171], v[26:29]
	v_mfma_f32_16x16x32_f16 v[58:61], v[212:215], v[172:175], v[26:29]
	v_mfma_f32_16x16x32_f16 v[26:29], v[130:133], v[176:179], v[154:157]
	v_mfma_f32_16x16x32_f16 v[46:49], v[204:207], v[146:149], v[26:29]
	v_mfma_f32_16x16x32_f16 v[26:29], v[208:211], v[176:179], v[158:161]
	v_mfma_f32_16x16x32_f16 v[10:13], v[208:211], v[184:187], v[10:13]
	v_mfma_f32_16x16x32_f16 v[30:33], v[130:133], v[168:171], v[30:33]
	v_mfma_f32_16x16x32_f16 v[42:45], v[212:215], v[146:149], v[26:29]
	v_mfma_f32_16x16x32_f16 v[14:17], v[130:133], v[184:187], v[14:17]
	v_mfma_f32_16x16x32_f16 v[26:29], v[212:215], v[200:203], v[10:13]
	v_mfma_f32_16x16x32_f16 v[10:13], v[130:133], v[224:227], v[164:167]
	v_mfma_f32_16x16x32_f16 v[62:65], v[204:207], v[172:175], v[30:33]
	v_mfma_f32_16x16x32_f16 v[30:33], v[204:207], v[200:203], v[14:17]
	v_mfma_f32_16x16x32_f16 v[14:17], v[204:207], v[228:231], v[10:13]
	v_mfma_f32_16x16x32_f16 v[10:13], v[208:211], v[224:227], v[188:191]
	v_mfma_f32_16x16x32_f16 v[10:13], v[212:215], v[228:231], v[10:13]
.Lg1_join:
	s_setprio 0
	s_movk_i32 s4, 0x100
	v_cmp_gt_u32_e32 vcc, s4, v141
	s_barrier
	s_and_saveexec_b64 s[4:5], vcc
	s_cbranch_execz .LBB2_385
	s_barrier

.Lg1p_loop:
	ds_read_b128 v[152:155], v151
	ds_read_b128 v[156:159], v151 offset:1024
	ds_read_b128 v[164:167], v151 offset:2048
	ds_read_b128 v[168:171], v151 offset:3072
	s_lshl_b32 s58, s84, 7
	s_add_u32 s59, s24, s58
	s_addc_u32 s91, s25, 0
	s_add_u32 s92, s59, 0x80
	s_addc_u32 s93, s91, 0
	s_add_i32 s56, s52, 0xc000
	s_mov_b32 m0, s56
	v_lshl_add_u64 v[160:161], s[92:93], 0, v[132:133]
	s_add_i32 s33, s52, 0xe000
	ds_read_b128 v[172:175], v147
	ds_read_b128 v[176:179], v147 offset:1024
	ds_read_b128 v[184:187], v146
	ds_read_b128 v[188:191], v146 offset:1024
	ds_read_b128 v[192:195], v145
	ds_read_b128 v[196:199], v145 offset:1024
	ds_read_b128 v[200:203], v144
	ds_read_b128 v[204:207], v144 offset:1024
	global_load_lds_dwordx4 v[160:161], off
	v_lshl_add_u64 v[160:161], s[92:93], 0, v[130:131]
	s_mov_b32 m0, s33
	s_nop 0
	global_load_lds_dwordx4 v[160:161], off
	s_waitcnt lgkmcnt(8)
	s_barrier
	s_waitcnt lgkmcnt(0)
	s_bitcmp1_b32 s100, 0
	s_cbranch_scc1 .Lg1p_skip1
	v_mfma_f32_16x16x32_f16 v[126:129], v[152:155], v[172:175], v[126:129]
	v_mfma_f32_16x16x32_f16 v[122:125], v[164:167], v[172:175], v[122:125]
	v_mfma_f32_16x16x32_f16 v[118:121], v[152:155], v[184:187], v[118:121]
	v_mfma_f32_16x16x32_f16 v[114:117], v[164:167], v[184:187], v[114:117]
	v_mfma_f32_16x16x32_f16 v[110:113], v[152:155], v[192:195], v[110:113]
	v_mfma_f32_16x16x32_f16 v[106:109], v[164:167], v[192:195], v[106:109]
	v_mfma_f32_16x16x32_f16 v[102:105], v[152:155], v[200:203], v[102:105]
	v_mfma_f32_16x16x32_f16 v[98:101], v[164:167], v[200:203], v[98:101]
	v_mfma_f32_16x16x32_f16 v[126:129], v[156:159], v[176:179], v[126:129]
	v_mfma_f32_16x16x32_f16 v[122:125], v[168:171], v[176:179], v[122:125]
	v_mfma_f32_16x16x32_f16 v[118:121], v[156:159], v[188:191], v[118:121]
	v_mfma_f32_16x16x32_f16 v[114:117], v[168:171], v[188:191], v[114:117]
	v_mfma_f32_16x16x32_f16 v[110:113], v[156:159], v[196:199], v[110:113]
	v_mfma_f32_16x16x32_f16 v[106:109], v[168:171], v[196:199], v[106:109]
	v_mfma_f32_16x16x32_f16 v[102:105], v[156:159], v[204:207], v[102:105]
	v_mfma_f32_16x16x32_f16 v[98:101], v[168:171], v[204:207], v[98:101]
.Lg1p_skip1:
	s_barrier
	s_add_i32 s57, s84, 2
	s_lshl_b32 s82, s57, 7
	s_add_u32 s92, s4, s82
	s_addc_u32 s93, s5, 0
	s_mov_b32 m0, s53
	v_lshl_add_u64 v[160:161], s[92:93], 0, v[162:163]
	s_add_u32 s92, s92, 0x40000
	s_addc_u32 s93, s93, 0
	ds_read_b128 v[208:211], v150
	ds_read_b128 v[212:215], v150 offset:1024
	ds_read_b128 v[216:219], v150 offset:2048
	ds_read_b128 v[220:223], v150 offset:3072
	global_load_lds_dwordx4 v[160:161], off
	s_mov_b32 m0, s55
	v_lshl_add_u64 v[160:161], s[92:93], 0, v[162:163]
	global_load_lds_dwordx4 v[160:161], off
	s_barrier
	s_waitcnt lgkmcnt(0)
	s_bitcmp1_b32 s100, 0
	s_cbranch_scc1 .Lg1p_skip2
	v_mfma_f32_16x16x32_f16 v[94:97], v[208:211], v[172:175], v[94:97]
	v_mfma_f32_16x16x32_f16 v[90:93], v[216:219], v[172:175], v[90:93]
	v_mfma_f32_16x16x32_f16 v[86:89], v[208:211], v[184:187], v[86:89]
	v_mfma_f32_16x16x32_f16 v[82:85], v[216:219], v[184:187], v[82:85]
	v_mfma_f32_16x16x32_f16 v[78:81], v[208:211], v[192:195], v[78:81]
	v_mfma_f32_16x16x32_f16 v[74:77], v[216:219], v[192:195], v[74:77]
	v_mfma_f32_16x16x32_f16 v[70:73], v[208:211], v[200:203], v[70:73]
	v_mfma_f32_16x16x32_f16 v[66:69], v[216:219], v[200:203], v[66:69]
	v_mfma_f32_16x16x32_f16 v[94:97], v[212:215], v[176:179], v[94:97]
	v_mfma_f32_16x16x32_f16 v[90:93], v[220:223], v[176:179], v[90:93]
	v_mfma_f32_16x16x32_f16 v[86:89], v[212:215], v[188:191], v[86:89]
	v_mfma_f32_16x16x32_f16 v[82:85], v[220:223], v[188:191], v[82:85]
	v_mfma_f32_16x16x32_f16 v[78:81], v[212:215], v[196:199], v[78:81]
	v_mfma_f32_16x16x32_f16 v[74:77], v[220:223], v[196:199], v[74:77]
	v_mfma_f32_16x16x32_f16 v[70:73], v[212:215], v[204:207], v[70:73]
	v_mfma_f32_16x16x32_f16 v[66:69], v[220:223], v[204:207], v[66:69]
.Lg1p_skip2:
	s_add_u32 s92, s24, s82
	s_addc_u32 s93, s25, 0
	s_mov_b32 m0, s52
	s_barrier
	v_lshl_add_u64 v[160:161], s[92:93], 0, v[134:135]
	ds_read_b128 v[172:175], v147 offset:16384
	ds_read_b128 v[176:179], v147 offset:17408
	ds_read_b128 v[184:187], v146 offset:16384
	ds_read_b128 v[188:191], v146 offset:17408
	ds_read_b128 v[192:195], v145 offset:16384
	ds_read_b128 v[196:199], v145 offset:17408
	ds_read_b128 v[200:203], v144 offset:16384
	ds_read_b128 v[204:207], v144 offset:17408
	global_load_lds_dwordx4 v[160:161], off
	v_lshl_add_u64 v[160:161], s[92:93], 0, v[136:137]
	s_mov_b32 m0, s86
	s_nop 0
	global_load_lds_dwordx4 v[160:161], off
	s_barrier
	s_waitcnt lgkmcnt(0)
	s_bitcmp1_b32 s100, 1
	s_cbranch_scc1 .Lg1p_skip3
	v_mfma_f32_16x16x32_f16 v[62:65], v[152:155], v[172:175], v[62:65]
	v_mfma_f32_16x16x32_f16 v[58:61], v[164:167], v[172:175], v[58:61]
	v_mfma_f32_16x16x32_f16 v[54:57], v[152:155], v[184:187], v[54:57]
	v_mfma_f32_16x16x32_f16 v[50:53], v[164:167], v[184:187], v[50:53]
	v_mfma_f32_16x16x32_f16 v[46:49], v[152:155], v[192:195], v[46:49]
	v_mfma_f32_16x16x32_f16 v[42:45], v[164:167], v[192:195], v[42:45]
	v_mfma_f32_16x16x32_f16 v[38:41], v[152:155], v[200:203], v[38:41]
	v_mfma_f32_16x16x32_f16 v[34:37], v[164:167], v[200:203], v[34:37]
	v_mfma_f32_16x16x32_f16 v[62:65], v[156:159], v[176:179], v[62:65]
	v_mfma_f32_16x16x32_f16 v[58:61], v[168:171], v[176:179], v[58:61]
	v_mfma_f32_16x16x32_f16 v[54:57], v[156:159], v[188:191], v[54:57]
	v_mfma_f32_16x16x32_f16 v[50:53], v[168:171], v[188:191], v[50:53]
	v_mfma_f32_16x16x32_f16 v[46:49], v[156:159], v[196:199], v[46:49]
	v_mfma_f32_16x16x32_f16 v[42:45], v[168:171], v[196:199], v[42:45]
	v_mfma_f32_16x16x32_f16 v[38:41], v[156:159], v[204:207], v[38:41]
	v_mfma_f32_16x16x32_f16 v[34:37], v[168:171], v[204:207], v[34:37]
.Lg1p_skip3:
	s_barrier
	s_add_u32 s94, s10, s82
	s_addc_u32 s95, s11, 0
	s_mov_b32 m0, s87
	v_lshl_add_u64 v[152:153], s[94:95], 0, v[162:163]
	s_add_u32 s94, s94, 0x40000
	s_addc_u32 s95, s95, 0
	global_load_lds_dwordx4 v[152:153], off
	s_mov_b32 m0, s88
	v_lshl_add_u64 v[152:153], s[94:95], 0, v[162:163]
	global_load_lds_dwordx4 v[152:153], off
	s_waitcnt vmcnt(6)
	s_barrier
	s_bitcmp1_b32 s100, 1
	s_cbranch_scc1 .Lg1p_skip4
	v_mfma_f32_16x16x32_f16 v[30:33], v[208:211], v[172:175], v[30:33]
	v_mfma_f32_16x16x32_f16 v[26:29], v[216:219], v[172:175], v[26:29]
	v_mfma_f32_16x16x32_f16 v[22:25], v[208:211], v[184:187], v[22:25]
	v_mfma_f32_16x16x32_f16 v[18:21], v[216:219], v[184:187], v[18:21]
	v_mfma_f32_16x16x32_f16 v[14:17], v[208:211], v[192:195], v[14:17]
	v_mfma_f32_16x16x32_f16 v[10:13], v[216:219], v[192:195], v[10:13]
	v_mfma_f32_16x16x32_f16 v[6:9], v[208:211], v[200:203], v[6:9]
	v_mfma_f32_16x16x32_f16 v[2:5], v[216:219], v[200:203], v[2:5]
	v_mfma_f32_16x16x32_f16 v[30:33], v[212:215], v[176:179], v[30:33]
	v_mfma_f32_16x16x32_f16 v[26:29], v[220:223], v[176:179], v[26:29]
	v_mfma_f32_16x16x32_f16 v[22:25], v[212:215], v[188:191], v[22:25]
	v_mfma_f32_16x16x32_f16 v[18:21], v[220:223], v[188:191], v[18:21]
	v_mfma_f32_16x16x32_f16 v[14:17], v[212:215], v[196:199], v[14:17]
	v_mfma_f32_16x16x32_f16 v[10:13], v[220:223], v[196:199], v[10:13]
	v_mfma_f32_16x16x32_f16 v[6:9], v[212:215], v[204:207], v[6:9]
	v_mfma_f32_16x16x32_f16 v[2:5], v[220:223], v[204:207], v[2:5]
.Lg1p_skip4:
	s_barrier
	ds_read_b128 v[152:155], v149
	ds_read_b128 v[156:159], v149 offset:1024
	ds_read_b128 v[164:167], v149 offset:2048
	ds_read_b128 v[168:171], v149 offset:3072
	s_mov_b32 m0, s89
	v_lshl_add_u64 v[160:161], s[92:93], 0, v[132:133]
	ds_read_b128 v[172:175], v147 offset:32768
	ds_read_b128 v[176:179], v147 offset:33792
	ds_read_b128 v[184:187], v146 offset:32768
	ds_read_b128 v[188:191], v146 offset:33792
	ds_read_b128 v[192:195], v145 offset:32768
	ds_read_b128 v[196:199], v145 offset:33792
	ds_read_b128 v[200:203], v144 offset:32768
	ds_read_b128 v[204:207], v144 offset:33792
	global_load_lds_dwordx4 v[160:161], off
	v_lshl_add_u64 v[160:161], s[92:93], 0, v[130:131]
	s_mov_b32 m0, s90
	s_nop 0
	global_load_lds_dwordx4 v[160:161], off
	s_waitcnt lgkmcnt(8)
	s_barrier
	s_waitcnt lgkmcnt(0)
	s_bitcmp1_b32 s100, 0
	s_cbranch_scc1 .Lg1p_skip5
	v_mfma_f32_16x16x32_f16 v[126:129], v[152:155], v[172:175], v[126:129]
	v_mfma_f32_16x16x32_f16 v[122:125], v[164:167], v[172:175], v[122:125]
	v_mfma_f32_16x16x32_f16 v[118:121], v[152:155], v[184:187], v[118:121]
	v_mfma_f32_16x16x32_f16 v[114:117], v[164:167], v[184:187], v[114:117]
	v_mfma_f32_16x16x32_f16 v[110:113], v[152:155], v[192:195], v[110:113]
	v_mfma_f32_16x16x32_f16 v[106:109], v[164:167], v[192:195], v[106:109]
	v_mfma_f32_16x16x32_f16 v[102:105], v[152:155], v[200:203], v[102:105]
	v_mfma_f32_16x16x32_f16 v[98:101], v[164:167], v[200:203], v[98:101]
	v_mfma_f32_16x16x32_f16 v[126:129], v[156:159], v[176:179], v[126:129]
	v_mfma_f32_16x16x32_f16 v[122:125], v[168:171], v[176:179], v[122:125]
	v_mfma_f32_16x16x32_f16 v[118:121], v[156:159], v[188:191], v[118:121]
	v_mfma_f32_16x16x32_f16 v[114:117], v[168:171], v[188:191], v[114:117]
	v_mfma_f32_16x16x32_f16 v[110:113], v[156:159], v[196:199], v[110:113]
	v_mfma_f32_16x16x32_f16 v[106:109], v[168:171], v[196:199], v[106:109]
	v_mfma_f32_16x16x32_f16 v[102:105], v[156:159], v[204:207], v[102:105]
	v_mfma_f32_16x16x32_f16 v[98:101], v[168:171], v[204:207], v[98:101]
.Lg1p_skip5:
	s_barrier
	s_add_u32 s82, s4, s58
	s_addc_u32 s83, s5, 0
	s_add_u32 s92, s82, 0x180
	s_addc_u32 s93, s83, 0
	s_add_i32 m0, s52, 0x18000
	v_lshl_add_u64 v[160:161], s[92:93], 0, v[162:163]
	s_add_u32 s92, s92, 0x40000
	s_addc_u32 s93, s93, 0
	ds_read_b128 v[208:211], v148
	ds_read_b128 v[212:215], v148 offset:1024
	ds_read_b128 v[216:219], v148 offset:2048
	ds_read_b128 v[220:223], v148 offset:3072
	global_load_lds_dwordx4 v[160:161], off
	s_add_i32 m0, s52, 0x1a000
	v_lshl_add_u64 v[160:161], s[92:93], 0, v[162:163]
	global_load_lds_dwordx4 v[160:161], off
	s_barrier
	s_waitcnt lgkmcnt(0)
	s_bitcmp1_b32 s100, 0
	s_cbranch_scc1 .Lg1p_skip6
	v_mfma_f32_16x16x32_f16 v[94:97], v[208:211], v[172:175], v[94:97]
	v_mfma_f32_16x16x32_f16 v[90:93], v[216:219], v[172:175], v[90:93]
	v_mfma_f32_16x16x32_f16 v[86:89], v[208:211], v[184:187], v[86:89]
	v_mfma_f32_16x16x32_f16 v[82:85], v[216:219], v[184:187], v[82:85]
	v_mfma_f32_16x16x32_f16 v[78:81], v[208:211], v[192:195], v[78:81]
	v_mfma_f32_16x16x32_f16 v[74:77], v[216:219], v[192:195], v[74:77]
	v_mfma_f32_16x16x32_f16 v[70:73], v[208:211], v[200:203], v[70:73]
	v_mfma_f32_16x16x32_f16 v[66:69], v[216:219], v[200:203], v[66:69]
	v_mfma_f32_16x16x32_f16 v[94:97], v[212:215], v[176:179], v[94:97]
	v_mfma_f32_16x16x32_f16 v[90:93], v[220:223], v[176:179], v[90:93]
	v_mfma_f32_16x16x32_f16 v[86:89], v[212:215], v[188:191], v[86:89]
	v_mfma_f32_16x16x32_f16 v[82:85], v[220:223], v[188:191], v[82:85]
	v_mfma_f32_16x16x32_f16 v[78:81], v[212:215], v[196:199], v[78:81]
	v_mfma_f32_16x16x32_f16 v[74:77], v[220:223], v[196:199], v[74:77]
	v_mfma_f32_16x16x32_f16 v[70:73], v[212:215], v[204:207], v[70:73]
	v_mfma_f32_16x16x32_f16 v[66:69], v[220:223], v[204:207], v[66:69]
.Lg1p_skip6:
	s_add_u32 s92, s59, 0x180
	s_addc_u32 s93, s91, 0
	s_mov_b32 m0, s34
	s_barrier
	v_lshl_add_u64 v[160:161], s[92:93], 0, v[134:135]
	ds_read_b128 v[172:175], v147 offset:49152
	ds_read_b128 v[176:179], v147 offset:50176
	ds_read_b128 v[184:187], v146 offset:49152
	ds_read_b128 v[188:191], v146 offset:50176
	ds_read_b128 v[192:195], v145 offset:49152
	ds_read_b128 v[196:199], v145 offset:50176
	ds_read_b128 v[200:203], v144 offset:49152
	ds_read_b128 v[204:207], v144 offset:50176
	global_load_lds_dwordx4 v[160:161], off
	v_lshl_add_u64 v[160:161], s[92:93], 0, v[136:137]
	s_mov_b32 m0, s35
	s_nop 0
	global_load_lds_dwordx4 v[160:161], off
	s_barrier
	s_waitcnt lgkmcnt(0)
	s_bitcmp1_b32 s100, 1
	s_cbranch_scc1 .Lg1p_skip7
	v_mfma_f32_16x16x32_f16 v[62:65], v[152:155], v[172:175], v[62:65]
	v_mfma_f32_16x16x32_f16 v[58:61], v[164:167], v[172:175], v[58:61]
	v_mfma_f32_16x16x32_f16 v[54:57], v[152:155], v[184:187], v[54:57]
	v_mfma_f32_16x16x32_f16 v[50:53], v[164:167], v[184:187], v[50:53]
	v_mfma_f32_16x16x32_f16 v[46:49], v[152:155], v[192:195], v[46:49]
	v_mfma_f32_16x16x32_f16 v[42:45], v[164:167], v[192:195], v[42:45]
	v_mfma_f32_16x16x32_f16 v[38:41], v[152:155], v[200:203], v[38:41]
	v_mfma_f32_16x16x32_f16 v[34:37], v[164:167], v[200:203], v[34:37]
	v_mfma_f32_16x16x32_f16 v[62:65], v[156:159], v[176:179], v[62:65]
	v_mfma_f32_16x16x32_f16 v[58:61], v[168:171], v[176:179], v[58:61]
	v_mfma_f32_16x16x32_f16 v[54:57], v[156:159], v[188:191], v[54:57]
	v_mfma_f32_16x16x32_f16 v[50:53], v[168:171], v[188:191], v[50:53]
	v_mfma_f32_16x16x32_f16 v[46:49], v[156:159], v[196:199], v[46:49]
	v_mfma_f32_16x16x32_f16 v[42:45], v[168:171], v[196:199], v[42:45]
	v_mfma_f32_16x16x32_f16 v[38:41], v[156:159], v[204:207], v[38:41]
	v_mfma_f32_16x16x32_f16 v[34:37], v[168:171], v[204:207], v[34:37]
.Lg1p_skip7:
	s_barrier
	s_add_u32 s58, s10, s58
	s_addc_u32 s59, s11, 0
	s_add_u32 s58, s58, 0x180
	s_addc_u32 s59, s59, 0
	s_add_i32 m0, s52, 0x1c000
	v_lshl_add_u64 v[152:153], s[58:59], 0, v[162:163]
	s_add_u32 s58, s58, 0x40000
	s_addc_u32 s59, s59, 0
	global_load_lds_dwordx4 v[152:153], off
	s_add_i32 m0, s52, 0x1e000
	v_lshl_add_u64 v[152:153], s[58:59], 0, v[162:163]
	global_load_lds_dwordx4 v[152:153], off
	s_waitcnt vmcnt(6)
	s_barrier
	s_bitcmp1_b32 s100, 1
	s_cbranch_scc1 .Lg1p_skip8
	v_mfma_f32_16x16x32_f16 v[30:33], v[208:211], v[172:175], v[30:33]
	v_mfma_f32_16x16x32_f16 v[26:29], v[216:219], v[172:175], v[26:29]
	v_mfma_f32_16x16x32_f16 v[22:25], v[208:211], v[184:187], v[22:25]
	v_mfma_f32_16x16x32_f16 v[18:21], v[216:219], v[184:187], v[18:21]
	v_mfma_f32_16x16x32_f16 v[14:17], v[208:211], v[192:195], v[14:17]
	v_mfma_f32_16x16x32_f16 v[10:13], v[216:219], v[192:195], v[10:13]
	v_mfma_f32_16x16x32_f16 v[6:9], v[208:211], v[200:203], v[6:9]
	v_mfma_f32_16x16x32_f16 v[2:5], v[216:219], v[200:203], v[2:5]
	v_mfma_f32_16x16x32_f16 v[30:33], v[212:215], v[176:179], v[30:33]
	v_mfma_f32_16x16x32_f16 v[26:29], v[220:223], v[176:179], v[26:29]
	v_mfma_f32_16x16x32_f16 v[22:25], v[212:215], v[188:191], v[22:25]
	v_mfma_f32_16x16x32_f16 v[18:21], v[220:223], v[188:191], v[18:21]
	v_mfma_f32_16x16x32_f16 v[14:17], v[212:215], v[196:199], v[14:17]
	v_mfma_f32_16x16x32_f16 v[10:13], v[220:223], v[196:199], v[10:13]
	v_mfma_f32_16x16x32_f16 v[6:9], v[212:215], v[204:207], v[6:9]
	v_mfma_f32_16x16x32_f16 v[2:5], v[220:223], v[204:207], v[2:5]
.Lg1p_skip8:
	s_cmp_lt_u32 s84, 28
	s_mov_b32 s84, s57
	s_barrier
	s_cbranch_scc1 .Lg1p_loop
	v_readlane_b32 s4, v244, 8
	v_readlane_b32 s5, v244, 9
	s_mov_b32 m0, s56
	ds_read_b128 v[134:137], v151
	ds_read_b128 v[152:155], v151 offset:1024
	ds_read_b128 v[156:159], v151 offset:2048
	ds_read_b128 v[164:167], v151 offset:3072
	ds_read_b128 v[168:171], v147
	ds_read_b128 v[172:175], v147 offset:1024
	ds_read_b128 v[176:179], v146
	ds_read_b128 v[184:187], v146 offset:1024
	ds_read_b128 v[188:191], v145
	ds_read_b128 v[192:195], v145 offset:1024
	ds_read_b128 v[196:199], v144
	ds_read_b128 v[200:203], v144 offset:1024
	v_lshl_add_u64 v[132:133], s[4:5], 0, v[132:133]
	global_load_lds_dwordx4 v[132:133], off
	v_lshl_add_u64 v[130:131], s[4:5], 0, v[130:131]
	s_mov_b32 m0, s33
	s_nop 0
	global_load_lds_dwordx4 v[130:131], off
	s_barrier
	s_waitcnt lgkmcnt(0)
	s_bitcmp1_b32 s100, 0
	s_cbranch_scc1 .Lg1p_skip9
	v_mfma_f32_16x16x32_f16 v[126:129], v[134:137], v[168:171], v[126:129]
	v_mfma_f32_16x16x32_f16 v[122:125], v[156:159], v[168:171], v[122:125]
	v_mfma_f32_16x16x32_f16 v[110:113], v[134:137], v[188:191], v[110:113]
	v_mfma_f32_16x16x32_f16 v[106:109], v[156:159], v[188:191], v[106:109]
	v_mfma_f32_16x16x32_f16 v[126:129], v[152:155], v[172:175], v[126:129]
	v_mfma_f32_16x16x32_f16 v[122:125], v[164:167], v[172:175], v[122:125]
	v_mfma_f32_16x16x32_f16 v[118:121], v[134:137], v[176:179], v[118:121]
	v_mfma_f32_16x16x32_f16 v[114:117], v[156:159], v[176:179], v[114:117]
	v_mfma_f32_16x16x32_f16 v[110:113], v[152:155], v[192:195], v[110:113]
	v_mfma_f32_16x16x32_f16 v[106:109], v[164:167], v[192:195], v[106:109]
	v_mfma_f32_16x16x32_f16 v[102:105], v[134:137], v[196:199], v[102:105]
	v_mfma_f32_16x16x32_f16 v[98:101], v[156:159], v[196:199], v[98:101]
	v_mfma_f32_16x16x32_f16 v[130:133], v[152:155], v[184:187], v[118:121]
	v_mfma_f32_16x16x32_f16 v[204:207], v[164:167], v[184:187], v[114:117]
	v_mfma_f32_16x16x32_f16 v[208:211], v[152:155], v[200:203], v[102:105]
	v_mfma_f32_16x16x32_f16 v[212:215], v[164:167], v[200:203], v[98:101]
.Lg1p_skip9:
	s_barrier
	s_nop 1
	ds_read_b128 v[98:101], v150
	ds_read_b128 v[102:105], v150 offset:1024
	ds_read_b128 v[114:117], v150 offset:2048
	ds_read_b128 v[118:121], v150 offset:3072
	s_barrier
	s_waitcnt lgkmcnt(0)
	s_bitcmp1_b32 s100, 0
	s_cbranch_scc1 .Lg1p_skip10
	v_mfma_f32_16x16x32_f16 v[94:97], v[98:101], v[168:171], v[94:97]
	v_mfma_f32_16x16x32_f16 v[90:93], v[114:117], v[168:171], v[90:93]
	v_mfma_f32_16x16x32_f16 v[78:81], v[98:101], v[188:191], v[78:81]
	v_mfma_f32_16x16x32_f16 v[74:77], v[114:117], v[188:191], v[74:77]
	v_mfma_f32_16x16x32_f16 v[94:97], v[102:105], v[172:175], v[94:97]
	v_mfma_f32_16x16x32_f16 v[90:93], v[118:121], v[172:175], v[90:93]
	v_mfma_f32_16x16x32_f16 v[86:89], v[98:101], v[176:179], v[86:89]
	v_mfma_f32_16x16x32_f16 v[82:85], v[114:117], v[176:179], v[82:85]
	v_mfma_f32_16x16x32_f16 v[78:81], v[102:105], v[192:195], v[78:81]
	v_mfma_f32_16x16x32_f16 v[74:77], v[118:121], v[192:195], v[74:77]
	v_mfma_f32_16x16x32_f16 v[70:73], v[98:101], v[196:199], v[70:73]
	v_mfma_f32_16x16x32_f16 v[66:69], v[114:117], v[196:199], v[66:69]
	v_mfma_f32_16x16x32_f16 v[168:171], v[102:105], v[184:187], v[86:89]
	v_mfma_f32_16x16x32_f16 v[172:175], v[118:121], v[184:187], v[82:85]
	v_mfma_f32_16x16x32_f16 v[176:179], v[102:105], v[200:203], v[70:73]
	v_mfma_f32_16x16x32_f16 v[184:187], v[118:121], v[200:203], v[66:69]
.Lg1p_skip10:
	s_barrier
	s_nop 1
	ds_read_b128 v[66:69], v147 offset:16384
	ds_read_b128 v[70:73], v147 offset:17408
	ds_read_b128 v[82:85], v146 offset:16384
	ds_read_b128 v[86:89], v146 offset:17408
	ds_read_b128 v[188:191], v145 offset:16384
	ds_read_b128 v[192:195], v145 offset:17408
	ds_read_b128 v[196:199], v144 offset:16384
	ds_read_b128 v[200:203], v144 offset:17408
	s_waitcnt vmcnt(4)
	s_barrier
	s_waitcnt lgkmcnt(0)
	s_bitcmp1_b32 s100, 1
	s_cbranch_scc1 .Lg1p_skip11
	v_mfma_f32_16x16x32_f16 v[62:65], v[134:137], v[66:69], v[62:65]
	v_mfma_f32_16x16x32_f16 v[58:61], v[156:159], v[66:69], v[58:61]
	v_mfma_f32_16x16x32_f16 v[46:49], v[134:137], v[188:191], v[46:49]
	v_mfma_f32_16x16x32_f16 v[42:45], v[156:159], v[188:191], v[42:45]
	v_mfma_f32_16x16x32_f16 v[62:65], v[152:155], v[70:73], v[62:65]
	v_mfma_f32_16x16x32_f16 v[58:61], v[164:167], v[70:73], v[58:61]
	v_mfma_f32_16x16x32_f16 v[54:57], v[134:137], v[82:85], v[54:57]
	v_mfma_f32_16x16x32_f16 v[50:53], v[156:159], v[82:85], v[50:53]
	v_mfma_f32_16x16x32_f16 v[46:49], v[152:155], v[192:195], v[46:49]
	v_mfma_f32_16x16x32_f16 v[42:45], v[164:167], v[192:195], v[42:45]
	v_mfma_f32_16x16x32_f16 v[38:41], v[134:137], v[196:199], v[38:41]
	v_mfma_f32_16x16x32_f16 v[34:37], v[156:159], v[196:199], v[34:37]
	v_mfma_f32_16x16x32_f16 v[216:219], v[152:155], v[86:89], v[54:57]
	v_mfma_f32_16x16x32_f16 v[220:223], v[164:167], v[86:89], v[50:53]
	v_mfma_f32_16x16x32_f16 v[134:137], v[152:155], v[200:203], v[38:41]
	v_mfma_f32_16x16x32_f16 v[150:153], v[164:167], v[200:203], v[34:37]
.Lg1p_skip11:
	s_bitcmp1_b32 s100, 1
	s_cbranch_scc1 .Lg1p_skip12
	v_mfma_f32_16x16x32_f16 v[30:33], v[98:101], v[66:69], v[30:33]
	v_mfma_f32_16x16x32_f16 v[26:29], v[114:117], v[66:69], v[26:29]
	v_mfma_f32_16x16x32_f16 v[14:17], v[98:101], v[188:191], v[14:17]
	v_mfma_f32_16x16x32_f16 v[10:13], v[114:117], v[188:191], v[10:13]
	v_mfma_f32_16x16x32_f16 v[30:33], v[102:105], v[70:73], v[30:33]
	v_mfma_f32_16x16x32_f16 v[26:29], v[118:121], v[70:73], v[26:29]
	v_mfma_f32_16x16x32_f16 v[22:25], v[98:101], v[82:85], v[22:25]
	v_mfma_f32_16x16x32_f16 v[18:21], v[114:117], v[82:85], v[18:21]
	v_mfma_f32_16x16x32_f16 v[14:17], v[102:105], v[192:195], v[14:17]
	v_mfma_f32_16x16x32_f16 v[10:13], v[118:121], v[192:195], v[10:13]
	v_mfma_f32_16x16x32_f16 v[6:9], v[98:101], v[196:199], v[6:9]
	v_mfma_f32_16x16x32_f16 v[2:5], v[114:117], v[196:199], v[2:5]
	v_mfma_f32_16x16x32_f16 v[154:157], v[102:105], v[86:89], v[22:25]
	v_mfma_f32_16x16x32_f16 v[158:161], v[118:121], v[86:89], v[18:21]
	v_mfma_f32_16x16x32_f16 v[164:167], v[102:105], v[200:203], v[6:9]
	v_mfma_f32_16x16x32_f16 v[188:191], v[118:121], v[200:203], v[2:5]
.Lg1p_skip12:
	s_barrier
	s_nop 1
	ds_read_b128 v[2:5], v149
	ds_read_b128 v[6:9], v149 offset:1024
	ds_read_b128 v[192:195], v149 offset:2048
	ds_read_b128 v[196:199], v149 offset:3072
	ds_read_b128 v[18:21], v147 offset:32768
	ds_read_b128 v[22:25], v147 offset:33792
	ds_read_b128 v[34:37], v146 offset:32768
	ds_read_b128 v[38:41], v146 offset:33792
	ds_read_b128 v[50:53], v145 offset:32768
	ds_read_b128 v[54:57], v145 offset:33792
	ds_read_b128 v[200:203], v144 offset:32768
	ds_read_b128 v[224:227], v144 offset:33792
	s_waitcnt vmcnt(2)
	s_barrier
	s_waitcnt lgkmcnt(0)
	s_bitcmp1_b32 s100, 0
	s_cbranch_scc1 .Lg1p_skip13
	v_mfma_f32_16x16x32_f16 v[66:69], v[2:5], v[18:21], v[126:129]
	v_mfma_f32_16x16x32_f16 v[118:121], v[6:9], v[22:25], v[66:69]
	v_mfma_f32_16x16x32_f16 v[66:69], v[192:195], v[18:21], v[122:125]
	v_mfma_f32_16x16x32_f16 v[114:117], v[196:199], v[22:25], v[66:69]
	v_mfma_f32_16x16x32_f16 v[66:69], v[2:5], v[34:37], v[130:133]
	v_mfma_f32_16x16x32_f16 v[102:105], v[6:9], v[38:41], v[66:69]
	v_mfma_f32_16x16x32_f16 v[66:69], v[192:195], v[34:37], v[204:207]
	v_mfma_f32_16x16x32_f16 v[98:101], v[196:199], v[38:41], v[66:69]
	v_mfma_f32_16x16x32_f16 v[66:69], v[2:5], v[50:53], v[110:113]
	v_mfma_f32_16x16x32_f16 v[86:89], v[6:9], v[54:57], v[66:69]
	v_mfma_f32_16x16x32_f16 v[66:69], v[192:195], v[50:53], v[106:109]
	v_mfma_f32_16x16x32_f16 v[82:85], v[196:199], v[54:57], v[66:69]
	v_mfma_f32_16x16x32_f16 v[66:69], v[2:5], v[200:203], v[208:211]
	v_mfma_f32_16x16x32_f16 v[70:73], v[6:9], v[224:227], v[66:69]
	v_mfma_f32_16x16x32_f16 v[66:69], v[192:195], v[200:203], v[212:215]
	v_mfma_f32_16x16x32_f16 v[66:69], v[196:199], v[224:227], v[66:69]
.Lg1p_skip13:
	s_barrier
	ds_read_b128 v[130:133], v148
	ds_read_b128 v[204:207], v148 offset:1024
	ds_read_b128 v[208:211], v148 offset:2048
	ds_read_b128 v[212:215], v148 offset:3072
	s_waitcnt vmcnt(0)
	s_barrier
	s_waitcnt lgkmcnt(0)
	s_bitcmp1_b32 s100, 0
	s_cbranch_scc1 .Lg1p_skip14
	v_mfma_f32_16x16x32_f16 v[94:97], v[130:133], v[18:21], v[94:97]
	v_mfma_f32_16x16x32_f16 v[18:21], v[208:211], v[18:21], v[90:93]
	v_mfma_f32_16x16x32_f16 v[122:125], v[212:215], v[22:25], v[18:21]
	v_mfma_f32_16x16x32_f16 v[18:21], v[130:133], v[34:37], v[168:171]
	v_mfma_f32_16x16x32_f16 v[110:113], v[204:207], v[38:41], v[18:21]
	v_mfma_f32_16x16x32_f16 v[18:21], v[208:211], v[34:37], v[172:175]
	v_mfma_f32_16x16x32_f16 v[106:109], v[212:215], v[38:41], v[18:21]
	v_mfma_f32_16x16x32_f16 v[18:21], v[130:133], v[50:53], v[78:81]
	v_mfma_f32_16x16x32_f16 v[126:129], v[204:207], v[22:25], v[94:97]
	v_mfma_f32_16x16x32_f16 v[94:97], v[204:207], v[54:57], v[18:21]
	v_mfma_f32_16x16x32_f16 v[18:21], v[208:211], v[50:53], v[74:77]
	v_mfma_f32_16x16x32_f16 v[90:93], v[212:215], v[54:57], v[18:21]
	v_mfma_f32_16x16x32_f16 v[18:21], v[130:133], v[200:203], v[176:179]
	v_mfma_f32_16x16x32_f16 v[78:81], v[204:207], v[224:227], v[18:21]
	v_mfma_f32_16x16x32_f16 v[18:21], v[208:211], v[200:203], v[184:187]
	v_mfma_f32_16x16x32_f16 v[74:77], v[212:215], v[224:227], v[18:21]
.Lg1p_skip14:
	s_barrier
	ds_read_b128 v[168:171], v147 offset:49152
	ds_read_b128 v[172:175], v147 offset:50176
	ds_read_b128 v[176:179], v146 offset:49152
	ds_read_b128 v[146:149], v146 offset:50176
	ds_read_b128 v[184:187], v145 offset:49152
	ds_read_b128 v[200:203], v145 offset:50176
	ds_read_b128 v[224:227], v144 offset:49152
	ds_read_b128 v[228:231], v144 offset:50176
	s_barrier
	s_waitcnt lgkmcnt(0)
	s_bitcmp1_b32 s100, 1
	s_cbranch_scc1 .Lg1p_skip15
	v_mfma_f32_16x16x32_f16 v[18:21], v[2:5], v[168:171], v[62:65]
	v_mfma_f32_16x16x32_f16 v[54:57], v[6:9], v[172:175], v[18:21]
	v_mfma_f32_16x16x32_f16 v[18:21], v[192:195], v[168:171], v[58:61]
	v_mfma_f32_16x16x32_f16 v[50:53], v[196:199], v[172:175], v[18:21]
	v_mfma_f32_16x16x32_f16 v[18:21], v[2:5], v[176:179], v[216:219]
	v_mfma_f32_16x16x32_f16 v[38:41], v[6:9], v[146:149], v[18:21]
	v_mfma_f32_16x16x32_f16 v[18:21], v[192:195], v[176:179], v[220:223]
	v_mfma_f32_16x16x32_f16 v[34:37], v[196:199], v[146:149], v[18:21]
	v_mfma_f32_16x16x32_f16 v[18:21], v[2:5], v[184:187], v[46:49]
	v_mfma_f32_16x16x32_f16 v[2:5], v[2:5], v[224:227], v[134:137]
	v_mfma_f32_16x16x32_f16 v[22:25], v[6:9], v[200:203], v[18:21]
	v_mfma_f32_16x16x32_f16 v[18:21], v[192:195], v[184:187], v[42:45]
	v_mfma_f32_16x16x32_f16 v[6:9], v[6:9], v[228:231], v[2:5]
	v_mfma_f32_16x16x32_f16 v[2:5], v[192:195], v[224:227], v[150:153]
	v_mfma_f32_16x16x32_f16 v[18:21], v[196:199], v[200:203], v[18:21]
	v_mfma_f32_16x16x32_f16 v[2:5], v[196:199], v[228:231], v[2:5]
.Lg1p_skip15:
	s_bitcmp1_b32 s100, 1
	s_cbranch_scc1 .Lg1p_skip16
	v_mfma_f32_16x16x32_f16 v[26:29], v[208:211], v[168:171], v[26:29]
	v_mfma_f32_16x16x32_f16 v[58:61], v[212:215], v[172:175], v[26:29]
	v_mfma_f32_16x16x32_f16 v[26:29], v[130:133], v[176:179], v[154:157]
	v_mfma_f32_16x16x32_f16 v[46:49], v[204:207], v[146:149], v[26:29]
	v_mfma_f32_16x16x32_f16 v[26:29], v[208:211], v[176:179], v[158:161]
	v_mfma_f32_16x16x32_f16 v[10:13], v[208:211], v[184:187], v[10:13]
	v_mfma_f32_16x16x32_f16 v[30:33], v[130:133], v[168:171], v[30:33]
	v_mfma_f32_16x16x32_f16 v[42:45], v[212:215], v[146:149], v[26:29]
	v_mfma_f32_16x16x32_f16 v[14:17], v[130:133], v[184:187], v[14:17]
	v_mfma_f32_16x16x32_f16 v[26:29], v[212:215], v[200:203], v[10:13]
	v_mfma_f32_16x16x32_f16 v[10:13], v[130:133], v[224:227], v[164:167]
	v_mfma_f32_16x16x32_f16 v[62:65], v[204:207], v[172:175], v[30:33]
	v_mfma_f32_16x16x32_f16 v[30:33], v[204:207], v[200:203], v[14:17]
	v_mfma_f32_16x16x32_f16 v[14:17], v[204:207], v[228:231], v[10:13]
	v_mfma_f32_16x16x32_f16 v[10:13], v[208:211], v[224:227], v[188:191]
	v_mfma_f32_16x16x32_f16 v[10:13], v[212:215], v[228:231], v[10:13]
.Lg1p_skip16:
	s_branch .Lg1_join
.Lg2p_loop:
	ds_read_b128 v[140:143], v138
	ds_read_b128 v[154:157], v138 offset:1024
	ds_read_b128 v[158:161], v138 offset:2048
	ds_read_b128 v[164:167], v138 offset:3072
	s_lshl_b32 vcc_hi, s57, 7
	s_add_u32 s58, s88, vcc_hi
	s_addc_u32 s59, s89, 0
	s_add_u32 s82, s58, 0x80
	s_addc_u32 s83, s59, 0
	s_add_i32 s59, s97, 0xc000
	v_lshl_add_u64 v[144:145], s[82:83], 0, v[162:163]
	s_add_u32 s82, s82, 0x20000
	s_mov_b32 m0, s59
	s_addc_u32 s83, s83, 0
	s_add_i32 s58, s97, 0xe000
	ds_read_b128 v[168:171], v134
	ds_read_b128 v[172:175], v134 offset:1024
	ds_read_b128 v[176:179], v133
	ds_read_b128 v[184:187], v133 offset:1024
	ds_read_b128 v[188:191], v131
	ds_read_b128 v[192:195], v131 offset:1024
	ds_read_b128 v[196:199], v130
	ds_read_b128 v[200:203], v130 offset:1024
	global_load_lds_dwordx4 v[144:145], off
	s_mov_b32 m0, s58
	v_lshl_add_u64 v[144:145], s[82:83], 0, v[162:163]
	global_load_lds_dwordx4 v[144:145], off
	s_waitcnt lgkmcnt(8)
	s_barrier
	s_waitcnt lgkmcnt(0)
	s_bitcmp1_b32 s100, 0
	s_cbranch_scc1 .Lg2p_skip1
	v_mfma_f32_16x16x32_f16 v[102:105], v[140:143], v[168:171], v[102:105]
	v_mfma_f32_16x16x32_f16 v[98:101], v[158:161], v[168:171], v[98:101]
	v_mfma_f32_16x16x32_f16 v[126:129], v[140:143], v[176:179], v[126:129]
	v_mfma_f32_16x16x32_f16 v[122:125], v[158:161], v[176:179], v[122:125]
	v_mfma_f32_16x16x32_f16 v[118:121], v[140:143], v[188:191], v[118:121]
	v_mfma_f32_16x16x32_f16 v[114:117], v[158:161], v[188:191], v[114:117]
	v_mfma_f32_16x16x32_f16 v[110:113], v[140:143], v[196:199], v[110:113]
	v_mfma_f32_16x16x32_f16 v[106:109], v[158:161], v[196:199], v[106:109]
	v_mfma_f32_16x16x32_f16 v[102:105], v[154:157], v[172:175], v[102:105]
	v_mfma_f32_16x16x32_f16 v[98:101], v[164:167], v[172:175], v[98:101]
	v_mfma_f32_16x16x32_f16 v[126:129], v[154:157], v[184:187], v[126:129]
	v_mfma_f32_16x16x32_f16 v[122:125], v[164:167], v[184:187], v[122:125]
	v_mfma_f32_16x16x32_f16 v[118:121], v[154:157], v[192:195], v[118:121]
	v_mfma_f32_16x16x32_f16 v[114:117], v[164:167], v[192:195], v[114:117]
	v_mfma_f32_16x16x32_f16 v[110:113], v[154:157], v[200:203], v[110:113]
	v_mfma_f32_16x16x32_f16 v[106:109], v[164:167], v[200:203], v[106:109]
.Lg2p_skip1:
	s_barrier
	s_add_i32 vcc_lo, s57, 2
	s_lshl_b32 s78, vcc_lo, 7
	s_add_u32 s82, s92, s78
	s_addc_u32 s83, s93, 0
	s_mov_b32 m0, s84
	v_lshl_add_u64 v[144:145], s[82:83], 0, v[162:163]
	s_add_u32 s82, s82, 0x20000
	s_addc_u32 s83, s83, 0
	ds_read_b128 v[204:207], v137
	ds_read_b128 v[208:211], v137 offset:1024
	ds_read_b128 v[212:215], v137 offset:2048
	ds_read_b128 v[216:219], v137 offset:3072
	global_load_lds_dwordx4 v[144:145], off
	s_mov_b32 m0, s94
	v_lshl_add_u64 v[144:145], s[82:83], 0, v[162:163]
	global_load_lds_dwordx4 v[144:145], off
	s_barrier
	s_waitcnt lgkmcnt(0)
	s_bitcmp1_b32 s100, 0
	s_cbranch_scc1 .Lg2p_skip2
	v_mfma_f32_16x16x32_f16 v[94:97], v[204:207], v[168:171], v[94:97]
	v_mfma_f32_16x16x32_f16 v[90:93], v[212:215], v[168:171], v[90:93]
	v_mfma_f32_16x16x32_f16 v[86:89], v[204:207], v[176:179], v[86:89]
	v_mfma_f32_16x16x32_f16 v[82:85], v[212:215], v[176:179], v[82:85]
	v_mfma_f32_16x16x32_f16 v[78:81], v[204:207], v[188:191], v[78:81]
	v_mfma_f32_16x16x32_f16 v[74:77], v[212:215], v[188:191], v[74:77]
	v_mfma_f32_16x16x32_f16 v[70:73], v[204:207], v[196:199], v[70:73]
	v_mfma_f32_16x16x32_f16 v[66:69], v[212:215], v[196:199], v[66:69]
	v_mfma_f32_16x16x32_f16 v[94:97], v[208:211], v[172:175], v[94:97]
	v_mfma_f32_16x16x32_f16 v[90:93], v[216:219], v[172:175], v[90:93]
	v_mfma_f32_16x16x32_f16 v[86:89], v[208:211], v[184:187], v[86:89]
	v_mfma_f32_16x16x32_f16 v[82:85], v[216:219], v[184:187], v[82:85]
	v_mfma_f32_16x16x32_f16 v[78:81], v[208:211], v[192:195], v[78:81]
	v_mfma_f32_16x16x32_f16 v[74:77], v[216:219], v[192:195], v[74:77]
	v_mfma_f32_16x16x32_f16 v[70:73], v[208:211], v[200:203], v[70:73]
	v_mfma_f32_16x16x32_f16 v[66:69], v[216:219], v[200:203], v[66:69]
.Lg2p_skip2:
	s_add_u32 s82, s90, s78
	s_addc_u32 s83, s91, 0
	s_mov_b32 m0, s97
	v_lshl_add_u64 v[144:145], s[82:83], 0, v[162:163]
	s_add_u32 s82, s82, 0x20000
	s_addc_u32 s83, s83, 0
	s_barrier
	ds_read_b128 v[168:171], v134 offset:16384
	ds_read_b128 v[172:175], v134 offset:17408
	ds_read_b128 v[176:179], v133 offset:16384
	ds_read_b128 v[184:187], v133 offset:17408
	ds_read_b128 v[188:191], v131 offset:16384
	ds_read_b128 v[192:195], v131 offset:17408
	ds_read_b128 v[196:199], v130 offset:16384
	ds_read_b128 v[200:203], v130 offset:17408
	global_load_lds_dwordx4 v[144:145], off
	s_mov_b32 m0, s99
	v_lshl_add_u64 v[144:145], s[82:83], 0, v[162:163]
	global_load_lds_dwordx4 v[144:145], off
	s_barrier
	s_waitcnt lgkmcnt(0)
	s_bitcmp1_b32 s100, 1
	s_cbranch_scc1 .Lg2p_skip3
	v_mfma_f32_16x16x32_f16 v[62:65], v[140:143], v[168:171], v[62:65]
	v_mfma_f32_16x16x32_f16 v[58:61], v[158:161], v[168:171], v[58:61]
	v_mfma_f32_16x16x32_f16 v[54:57], v[140:143], v[176:179], v[54:57]
	v_mfma_f32_16x16x32_f16 v[50:53], v[158:161], v[176:179], v[50:53]
	v_mfma_f32_16x16x32_f16 v[46:49], v[140:143], v[188:191], v[46:49]
	v_mfma_f32_16x16x32_f16 v[42:45], v[158:161], v[188:191], v[42:45]
	v_mfma_f32_16x16x32_f16 v[38:41], v[140:143], v[196:199], v[38:41]
	v_mfma_f32_16x16x32_f16 v[30:33], v[158:161], v[196:199], v[30:33]
	v_mfma_f32_16x16x32_f16 v[62:65], v[154:157], v[172:175], v[62:65]
	v_mfma_f32_16x16x32_f16 v[58:61], v[164:167], v[172:175], v[58:61]
	v_mfma_f32_16x16x32_f16 v[54:57], v[154:157], v[184:187], v[54:57]
	v_mfma_f32_16x16x32_f16 v[50:53], v[164:167], v[184:187], v[50:53]
	v_mfma_f32_16x16x32_f16 v[46:49], v[154:157], v[192:195], v[46:49]
	v_mfma_f32_16x16x32_f16 v[42:45], v[164:167], v[192:195], v[42:45]
	v_mfma_f32_16x16x32_f16 v[38:41], v[154:157], v[200:203], v[38:41]
	v_mfma_f32_16x16x32_f16 v[30:33], v[164:167], v[200:203], v[30:33]
.Lg2p_skip3:
	s_barrier
	s_add_u32 s82, s34, s78
	s_addc_u32 s83, s35, 0
	s_mov_b32 m0, s95
	v_lshl_add_u64 v[140:141], s[82:83], 0, v[162:163]
	s_add_u32 s82, s82, 0x20000
	s_addc_u32 s83, s83, 0
	global_load_lds_dwordx4 v[140:141], off
	s_mov_b32 m0, s33
	v_lshl_add_u64 v[140:141], s[82:83], 0, v[162:163]
	global_load_lds_dwordx4 v[140:141], off
	s_waitcnt vmcnt(6)
	s_barrier
	s_bitcmp1_b32 s100, 1
	s_cbranch_scc1 .Lg2p_skip4
	v_mfma_f32_16x16x32_f16 v[34:37], v[204:207], v[168:171], v[34:37]
	v_mfma_f32_16x16x32_f16 v[26:29], v[212:215], v[168:171], v[26:29]
	v_mfma_f32_16x16x32_f16 v[22:25], v[204:207], v[176:179], v[22:25]
	v_mfma_f32_16x16x32_f16 v[18:21], v[212:215], v[176:179], v[18:21]
	v_mfma_f32_16x16x32_f16 v[14:17], v[204:207], v[188:191], v[14:17]
	v_mfma_f32_16x16x32_f16 v[10:13], v[212:215], v[188:191], v[10:13]
	v_mfma_f32_16x16x32_f16 v[6:9], v[204:207], v[196:199], v[6:9]
	v_mfma_f32_16x16x32_f16 v[2:5], v[212:215], v[196:199], v[2:5]
	v_mfma_f32_16x16x32_f16 v[34:37], v[208:211], v[172:175], v[34:37]
	v_mfma_f32_16x16x32_f16 v[26:29], v[216:219], v[172:175], v[26:29]
	v_mfma_f32_16x16x32_f16 v[22:25], v[208:211], v[184:187], v[22:25]
	v_mfma_f32_16x16x32_f16 v[18:21], v[216:219], v[184:187], v[18:21]
	v_mfma_f32_16x16x32_f16 v[14:17], v[208:211], v[192:195], v[14:17]
	v_mfma_f32_16x16x32_f16 v[10:13], v[216:219], v[192:195], v[10:13]
	v_mfma_f32_16x16x32_f16 v[6:9], v[208:211], v[200:203], v[6:9]
	v_mfma_f32_16x16x32_f16 v[2:5], v[216:219], v[200:203], v[2:5]
.Lg2p_skip4:
	s_barrier
	ds_read_b128 v[140:143], v136
	ds_read_b128 v[154:157], v136 offset:1024
	ds_read_b128 v[158:161], v136 offset:2048
	ds_read_b128 v[164:167], v136 offset:3072
	s_add_u32 s82, s88, s78
	s_addc_u32 s83, s89, 0
	s_mov_b32 m0, s11
	v_lshl_add_u64 v[144:145], s[82:83], 0, v[162:163]
	s_add_u32 s82, s82, 0x20000
	s_addc_u32 s83, s83, 0
	ds_read_b128 v[168:171], v134 offset:32768
	ds_read_b128 v[172:175], v134 offset:33792
	ds_read_b128 v[176:179], v133 offset:32768
	ds_read_b128 v[184:187], v133 offset:33792
	ds_read_b128 v[188:191], v131 offset:32768
	ds_read_b128 v[192:195], v131 offset:33792
	ds_read_b128 v[196:199], v130 offset:32768
	ds_read_b128 v[200:203], v130 offset:33792
	global_load_lds_dwordx4 v[144:145], off
	s_mov_b32 m0, s56
	v_lshl_add_u64 v[144:145], s[82:83], 0, v[162:163]
	global_load_lds_dwordx4 v[144:145], off
	s_waitcnt lgkmcnt(8)
	s_barrier
	s_waitcnt lgkmcnt(0)
	s_bitcmp1_b32 s100, 0
	s_cbranch_scc1 .Lg2p_skip5
	v_mfma_f32_16x16x32_f16 v[102:105], v[140:143], v[168:171], v[102:105]
	v_mfma_f32_16x16x32_f16 v[98:101], v[158:161], v[168:171], v[98:101]
	v_mfma_f32_16x16x32_f16 v[126:129], v[140:143], v[176:179], v[126:129]
	v_mfma_f32_16x16x32_f16 v[122:125], v[158:161], v[176:179], v[122:125]
	v_mfma_f32_16x16x32_f16 v[118:121], v[140:143], v[188:191], v[118:121]
	v_mfma_f32_16x16x32_f16 v[114:117], v[158:161], v[188:191], v[114:117]
	v_mfma_f32_16x16x32_f16 v[110:113], v[140:143], v[196:199], v[110:113]
	v_mfma_f32_16x16x32_f16 v[106:109], v[158:161], v[196:199], v[106:109]
	v_mfma_f32_16x16x32_f16 v[102:105], v[154:157], v[172:175], v[102:105]
	v_mfma_f32_16x16x32_f16 v[98:101], v[164:167], v[172:175], v[98:101]
	v_mfma_f32_16x16x32_f16 v[126:129], v[154:157], v[184:187], v[126:129]
	v_mfma_f32_16x16x32_f16 v[122:125], v[164:167], v[184:187], v[122:125]
	v_mfma_f32_16x16x32_f16 v[118:121], v[154:157], v[192:195], v[118:121]
	v_mfma_f32_16x16x32_f16 v[114:117], v[164:167], v[192:195], v[114:117]
	v_mfma_f32_16x16x32_f16 v[110:113], v[154:157], v[200:203], v[110:113]
	v_mfma_f32_16x16x32_f16 v[106:109], v[164:167], v[200:203], v[106:109]
.Lg2p_skip5:
	s_barrier
	s_add_u32 s78, s92, vcc_hi
	s_addc_u32 s79, s93, 0
	s_add_u32 s82, s78, 0x180
	s_addc_u32 s83, s79, 0
	s_add_i32 m0, s97, 0x18000
	v_lshl_add_u64 v[144:145], s[82:83], 0, v[162:163]
	s_add_u32 s82, s82, 0x20000
	s_addc_u32 s83, s83, 0
	ds_read_b128 v[204:207], v135
	ds_read_b128 v[208:211], v135 offset:1024
	ds_read_b128 v[212:215], v135 offset:2048
	ds_read_b128 v[216:219], v135 offset:3072
	global_load_lds_dwordx4 v[144:145], off
	s_add_i32 m0, s97, 0x1a000
	v_lshl_add_u64 v[144:145], s[82:83], 0, v[162:163]
	global_load_lds_dwordx4 v[144:145], off
	s_barrier
	s_waitcnt lgkmcnt(0)
	s_bitcmp1_b32 s100, 0
	s_cbranch_scc1 .Lg2p_skip6
	v_mfma_f32_16x16x32_f16 v[94:97], v[204:207], v[168:171], v[94:97]
	v_mfma_f32_16x16x32_f16 v[90:93], v[212:215], v[168:171], v[90:93]
	v_mfma_f32_16x16x32_f16 v[86:89], v[204:207], v[176:179], v[86:89]
	v_mfma_f32_16x16x32_f16 v[82:85], v[212:215], v[176:179], v[82:85]
	v_mfma_f32_16x16x32_f16 v[78:81], v[204:207], v[188:191], v[78:81]
	v_mfma_f32_16x16x32_f16 v[74:77], v[212:215], v[188:191], v[74:77]
	v_mfma_f32_16x16x32_f16 v[70:73], v[204:207], v[196:199], v[70:73]
	v_mfma_f32_16x16x32_f16 v[66:69], v[212:215], v[196:199], v[66:69]
	v_mfma_f32_16x16x32_f16 v[94:97], v[208:211], v[172:175], v[94:97]
	v_mfma_f32_16x16x32_f16 v[90:93], v[216:219], v[172:175], v[90:93]
	v_mfma_f32_16x16x32_f16 v[86:89], v[208:211], v[184:187], v[86:89]
	v_mfma_f32_16x16x32_f16 v[82:85], v[216:219], v[184:187], v[82:85]
	v_mfma_f32_16x16x32_f16 v[78:81], v[208:211], v[192:195], v[78:81]
	v_mfma_f32_16x16x32_f16 v[74:77], v[216:219], v[192:195], v[74:77]
	v_mfma_f32_16x16x32_f16 v[70:73], v[208:211], v[200:203], v[70:73]
	v_mfma_f32_16x16x32_f16 v[66:69], v[216:219], v[200:203], v[66:69]
.Lg2p_skip6:
	s_add_u32 s78, s90, vcc_hi
	s_addc_u32 s79, s91, 0
	s_add_u32 s82, s78, 0x180
	s_addc_u32 s83, s79, 0
	s_mov_b32 m0, s52
	v_lshl_add_u64 v[144:145], s[82:83], 0, v[162:163]
	s_add_u32 s82, s82, 0x20000
	s_addc_u32 s83, s83, 0
	s_barrier
	ds_read_b128 v[168:171], v134 offset:49152
	ds_read_b128 v[172:175], v134 offset:50176
	ds_read_b128 v[176:179], v133 offset:49152
	ds_read_b128 v[184:187], v133 offset:50176
	ds_read_b128 v[188:191], v131 offset:49152
	ds_read_b128 v[192:195], v131 offset:50176
	ds_read_b128 v[196:199], v130 offset:49152
	ds_read_b128 v[200:203], v130 offset:50176
	global_load_lds_dwordx4 v[144:145], off
	s_mov_b32 m0, s53
	v_lshl_add_u64 v[144:145], s[82:83], 0, v[162:163]
	global_load_lds_dwordx4 v[144:145], off
	s_barrier
	s_waitcnt lgkmcnt(0)
	s_bitcmp1_b32 s100, 1
	s_cbranch_scc1 .Lg2p_skip7
	v_mfma_f32_16x16x32_f16 v[62:65], v[140:143], v[168:171], v[62:65]
	v_mfma_f32_16x16x32_f16 v[58:61], v[158:161], v[168:171], v[58:61]
	v_mfma_f32_16x16x32_f16 v[54:57], v[140:143], v[176:179], v[54:57]
	v_mfma_f32_16x16x32_f16 v[50:53], v[158:161], v[176:179], v[50:53]
	v_mfma_f32_16x16x32_f16 v[46:49], v[140:143], v[188:191], v[46:49]
	v_mfma_f32_16x16x32_f16 v[42:45], v[158:161], v[188:191], v[42:45]
	v_mfma_f32_16x16x32_f16 v[38:41], v[140:143], v[196:199], v[38:41]
	v_mfma_f32_16x16x32_f16 v[30:33], v[158:161], v[196:199], v[30:33]
	v_mfma_f32_16x16x32_f16 v[62:65], v[154:157], v[172:175], v[62:65]
	v_mfma_f32_16x16x32_f16 v[58:61], v[164:167], v[172:175], v[58:61]
	v_mfma_f32_16x16x32_f16 v[54:57], v[154:157], v[184:187], v[54:57]
	v_mfma_f32_16x16x32_f16 v[50:53], v[164:167], v[184:187], v[50:53]
	v_mfma_f32_16x16x32_f16 v[46:49], v[154:157], v[192:195], v[46:49]
	v_mfma_f32_16x16x32_f16 v[42:45], v[164:167], v[192:195], v[42:45]
	v_mfma_f32_16x16x32_f16 v[38:41], v[154:157], v[200:203], v[38:41]
	v_mfma_f32_16x16x32_f16 v[30:33], v[164:167], v[200:203], v[30:33]
.Lg2p_skip7:
	s_barrier
	s_add_u32 s78, s34, vcc_hi
	s_addc_u32 s79, s35, 0
	s_add_u32 s82, s78, 0x180
	s_addc_u32 s83, s79, 0
	s_add_i32 m0, s97, 0x1c000
	v_lshl_add_u64 v[140:141], s[82:83], 0, v[162:163]
	s_add_u32 s82, s82, 0x20000
	s_addc_u32 s83, s83, 0
	global_load_lds_dwordx4 v[140:141], off
	s_add_i32 m0, s97, 0x1e000
	v_lshl_add_u64 v[140:141], s[82:83], 0, v[162:163]
	global_load_lds_dwordx4 v[140:141], off
	s_waitcnt vmcnt(6)
	s_barrier
	s_bitcmp1_b32 s100, 1
	s_cbranch_scc1 .Lg2p_skip8
	v_mfma_f32_16x16x32_f16 v[34:37], v[204:207], v[168:171], v[34:37]
	v_mfma_f32_16x16x32_f16 v[26:29], v[212:215], v[168:171], v[26:29]
	v_mfma_f32_16x16x32_f16 v[22:25], v[204:207], v[176:179], v[22:25]
	v_mfma_f32_16x16x32_f16 v[18:21], v[212:215], v[176:179], v[18:21]
	v_mfma_f32_16x16x32_f16 v[14:17], v[204:207], v[188:191], v[14:17]
	v_mfma_f32_16x16x32_f16 v[10:13], v[212:215], v[188:191], v[10:13]
	v_mfma_f32_16x16x32_f16 v[6:9], v[204:207], v[196:199], v[6:9]
	v_mfma_f32_16x16x32_f16 v[2:5], v[212:215], v[196:199], v[2:5]
	v_mfma_f32_16x16x32_f16 v[34:37], v[208:211], v[172:175], v[34:37]
	v_mfma_f32_16x16x32_f16 v[26:29], v[216:219], v[172:175], v[26:29]
	v_mfma_f32_16x16x32_f16 v[22:25], v[208:211], v[184:187], v[22:25]
	v_mfma_f32_16x16x32_f16 v[18:21], v[216:219], v[184:187], v[18:21]
	v_mfma_f32_16x16x32_f16 v[14:17], v[208:211], v[192:195], v[14:17]
	v_mfma_f32_16x16x32_f16 v[10:13], v[216:219], v[192:195], v[10:13]
	v_mfma_f32_16x16x32_f16 v[6:9], v[208:211], v[200:203], v[6:9]
	v_mfma_f32_16x16x32_f16 v[2:5], v[216:219], v[200:203], v[2:5]
.Lg2p_skip8:
	s_cmp_lt_u32 s57, 12
	s_mov_b32 s57, vcc_lo
	s_barrier
	s_cbranch_scc1 .Lg2p_loop
	s_add_u32 s34, s88, 0x780
	s_addc_u32 s35, s89, 0
	ds_read_b128 v[140:143], v138
	ds_read_b128 v[154:157], v138 offset:1024
	ds_read_b128 v[158:161], v138 offset:2048
	ds_read_b128 v[164:167], v138 offset:3072
	ds_read_b128 v[168:171], v134
	ds_read_b128 v[172:175], v134 offset:1024
	ds_read_b128 v[176:179], v133
	ds_read_b128 v[184:187], v133 offset:1024
	ds_read_b128 v[188:191], v131
	ds_read_b128 v[192:195], v131 offset:1024
	ds_read_b128 v[196:199], v130
	ds_read_b128 v[200:203], v130 offset:1024
	v_lshl_add_u64 v[138:139], s[34:35], 0, v[162:163]
	s_add_u32 s34, s34, 0x20000
	s_mov_b32 m0, s59
	s_addc_u32 s35, s35, 0
	global_load_lds_dwordx4 v[138:139], off
	s_mov_b32 m0, s58
	v_lshl_add_u64 v[138:139], s[34:35], 0, v[162:163]
	global_load_lds_dwordx4 v[138:139], off
	s_barrier
	s_waitcnt lgkmcnt(0)
	s_bitcmp1_b32 s100, 0
	s_cbranch_scc1 .Lg2p_skip9
	v_mfma_f32_16x16x32_f16 v[102:105], v[140:143], v[168:171], v[102:105]
	v_mfma_f32_16x16x32_f16 v[98:101], v[158:161], v[168:171], v[98:101]
	v_mfma_f32_16x16x32_f16 v[126:129], v[140:143], v[176:179], v[126:129]
	v_mfma_f32_16x16x32_f16 v[122:125], v[158:161], v[176:179], v[122:125]
	v_mfma_f32_16x16x32_f16 v[118:121], v[140:143], v[188:191], v[118:121]
	v_mfma_f32_16x16x32_f16 v[114:117], v[158:161], v[188:191], v[114:117]
	v_mfma_f32_16x16x32_f16 v[110:113], v[140:143], v[196:199], v[110:113]
	v_mfma_f32_16x16x32_f16 v[106:109], v[158:161], v[196:199], v[106:109]
	v_mfma_f32_16x16x32_f16 v[102:105], v[154:157], v[172:175], v[102:105]
	v_mfma_f32_16x16x32_f16 v[98:101], v[164:167], v[172:175], v[98:101]
	v_mfma_f32_16x16x32_f16 v[126:129], v[154:157], v[184:187], v[126:129]
	v_mfma_f32_16x16x32_f16 v[122:125], v[164:167], v[184:187], v[122:125]
	v_mfma_f32_16x16x32_f16 v[118:121], v[154:157], v[192:195], v[118:121]
	v_mfma_f32_16x16x32_f16 v[114:117], v[164:167], v[192:195], v[114:117]
	v_mfma_f32_16x16x32_f16 v[110:113], v[154:157], v[200:203], v[110:113]
	v_mfma_f32_16x16x32_f16 v[106:109], v[164:167], v[200:203], v[106:109]
.Lg2p_skip9:
	s_barrier
	ds_read_b128 v[204:207], v137
	ds_read_b128 v[208:211], v137 offset:1024
	ds_read_b128 v[212:215], v137 offset:2048
	ds_read_b128 v[216:219], v137 offset:3072
	s_barrier
	s_waitcnt lgkmcnt(0)
	s_bitcmp1_b32 s100, 0
	s_cbranch_scc1 .Lg2p_skip10
	v_mfma_f32_16x16x32_f16 v[94:97], v[204:207], v[168:171], v[94:97]
	v_mfma_f32_16x16x32_f16 v[94:97], v[208:211], v[172:175], v[94:97]
	v_mfma_f32_16x16x32_f16 v[90:93], v[212:215], v[168:171], v[90:93]
	v_mfma_f32_16x16x32_f16 v[86:89], v[204:207], v[176:179], v[86:89]
	v_mfma_f32_16x16x32_f16 v[82:85], v[212:215], v[176:179], v[82:85]
	v_mfma_f32_16x16x32_f16 v[78:81], v[204:207], v[188:191], v[78:81]
	v_mfma_f32_16x16x32_f16 v[74:77], v[212:215], v[188:191], v[74:77]
	v_mfma_f32_16x16x32_f16 v[70:73], v[204:207], v[196:199], v[70:73]
	v_mfma_f32_16x16x32_f16 v[66:69], v[212:215], v[196:199], v[66:69]
	v_mfma_f32_16x16x32_f16 v[168:171], v[216:219], v[172:175], v[90:93]
	v_mfma_f32_16x16x32_f16 v[172:175], v[208:211], v[184:187], v[86:89]
	v_mfma_f32_16x16x32_f16 v[176:179], v[216:219], v[184:187], v[82:85]
	v_mfma_f32_16x16x32_f16 v[184:187], v[208:211], v[192:195], v[78:81]
	v_mfma_f32_16x16x32_f16 v[188:191], v[216:219], v[192:195], v[74:77]
	v_mfma_f32_16x16x32_f16 v[192:195], v[208:211], v[200:203], v[70:73]
	v_mfma_f32_16x16x32_f16 v[196:199], v[216:219], v[200:203], v[66:69]
.Lg2p_skip10:
	s_barrier
	s_nop 0
	ds_read_b128 v[66:69], v134 offset:16384
	ds_read_b128 v[70:73], v134 offset:17408
	ds_read_b128 v[74:77], v133 offset:16384
	ds_read_b128 v[78:81], v133 offset:17408
	ds_read_b128 v[82:85], v131 offset:16384
	ds_read_b128 v[86:89], v131 offset:17408
	ds_read_b128 v[90:93], v130 offset:16384
	ds_read_b128 v[200:203], v130 offset:17408
	s_waitcnt vmcnt(4)
	s_barrier
	s_waitcnt lgkmcnt(0)
	s_bitcmp1_b32 s100, 1
	s_cbranch_scc1 .Lg2p_skip11
	v_mfma_f32_16x16x32_f16 v[62:65], v[140:143], v[66:69], v[62:65]
	v_mfma_f32_16x16x32_f16 v[58:61], v[158:161], v[66:69], v[58:61]
	v_mfma_f32_16x16x32_f16 v[54:57], v[140:143], v[74:77], v[54:57]
	v_mfma_f32_16x16x32_f16 v[50:53], v[158:161], v[74:77], v[50:53]
	v_mfma_f32_16x16x32_f16 v[46:49], v[140:143], v[82:85], v[46:49]
	v_mfma_f32_16x16x32_f16 v[42:45], v[158:161], v[82:85], v[42:45]
	v_mfma_f32_16x16x32_f16 v[38:41], v[140:143], v[90:93], v[38:41]
	v_mfma_f32_16x16x32_f16 v[62:65], v[154:157], v[70:73], v[62:65]
	v_mfma_f32_16x16x32_f16 v[58:61], v[164:167], v[70:73], v[58:61]
	v_mfma_f32_16x16x32_f16 v[54:57], v[154:157], v[78:81], v[54:57]
	v_mfma_f32_16x16x32_f16 v[50:53], v[164:167], v[78:81], v[50:53]
	v_mfma_f32_16x16x32_f16 v[46:49], v[154:157], v[86:89], v[46:49]
	v_mfma_f32_16x16x32_f16 v[42:45], v[164:167], v[86:89], v[42:45]
	v_mfma_f32_16x16x32_f16 v[38:41], v[154:157], v[200:203], v[38:41]
	v_mfma_f32_16x16x32_f16 v[30:33], v[158:161], v[90:93], v[30:33]
	v_mfma_f32_16x16x32_f16 v[138:141], v[164:167], v[200:203], v[30:33]
.Lg2p_skip11:
	s_bitcmp1_b32 s100, 1
	s_cbranch_scc1 .Lg2p_skip12
	v_mfma_f32_16x16x32_f16 v[30:33], v[204:207], v[66:69], v[34:37]
	v_mfma_f32_16x16x32_f16 v[34:37], v[208:211], v[70:73], v[30:33]
	v_mfma_f32_16x16x32_f16 v[26:29], v[212:215], v[66:69], v[26:29]
	v_mfma_f32_16x16x32_f16 v[22:25], v[204:207], v[74:77], v[22:25]
	v_mfma_f32_16x16x32_f16 v[18:21], v[212:215], v[74:77], v[18:21]
	v_mfma_f32_16x16x32_f16 v[14:17], v[204:207], v[82:85], v[14:17]
	v_mfma_f32_16x16x32_f16 v[10:13], v[212:215], v[82:85], v[10:13]
	v_mfma_f32_16x16x32_f16 v[6:9], v[204:207], v[90:93], v[6:9]
	v_mfma_f32_16x16x32_f16 v[2:5], v[212:215], v[90:93], v[2:5]
	v_mfma_f32_16x16x32_f16 v[142:145], v[216:219], v[70:73], v[26:29]
	v_mfma_f32_16x16x32_f16 v[154:157], v[208:211], v[78:81], v[22:25]
	v_mfma_f32_16x16x32_f16 v[158:161], v[216:219], v[78:81], v[18:21]
	v_mfma_f32_16x16x32_f16 v[164:167], v[208:211], v[86:89], v[14:17]
	v_mfma_f32_16x16x32_f16 v[220:223], v[216:219], v[86:89], v[10:13]
	v_mfma_f32_16x16x32_f16 v[204:207], v[208:211], v[200:203], v[6:9]
	v_mfma_f32_16x16x32_f16 v[200:203], v[216:219], v[200:203], v[2:5]
.Lg2p_skip12:
	s_barrier
	s_nop 0
	ds_read_b128 v[2:5], v136
	ds_read_b128 v[6:9], v136 offset:1024
	ds_read_b128 v[208:211], v136 offset:2048
	ds_read_b128 v[212:215], v136 offset:3072
	ds_read_b128 v[10:13], v134 offset:32768
	ds_read_b128 v[14:17], v134 offset:33792
	ds_read_b128 v[18:21], v133 offset:32768
	ds_read_b128 v[22:25], v133 offset:33792
	ds_read_b128 v[26:29], v131 offset:32768
	ds_read_b128 v[30:33], v131 offset:33792
	ds_read_b128 v[216:219], v130 offset:32768
	ds_read_b128 v[224:227], v130 offset:33792
	s_waitcnt vmcnt(2)
	s_barrier
	s_waitcnt lgkmcnt(0)
	s_bitcmp1_b32 s100, 0
	s_cbranch_scc1 .Lg2p_skip13
	v_mfma_f32_16x16x32_f16 v[66:69], v[2:5], v[10:13], v[102:105]
	v_mfma_f32_16x16x32_f16 v[90:93], v[6:9], v[14:17], v[66:69]
	v_mfma_f32_16x16x32_f16 v[66:69], v[208:211], v[10:13], v[98:101]
	v_mfma_f32_16x16x32_f16 v[98:101], v[212:215], v[14:17], v[66:69]
	v_mfma_f32_16x16x32_f16 v[66:69], v[2:5], v[18:21], v[126:129]
	v_mfma_f32_16x16x32_f16 v[82:85], v[6:9], v[22:25], v[66:69]
	v_mfma_f32_16x16x32_f16 v[66:69], v[208:211], v[18:21], v[122:125]
	v_mfma_f32_16x16x32_f16 v[86:89], v[212:215], v[22:25], v[66:69]
	v_mfma_f32_16x16x32_f16 v[66:69], v[2:5], v[26:29], v[118:121]
	v_mfma_f32_16x16x32_f16 v[74:77], v[6:9], v[30:33], v[66:69]
	v_mfma_f32_16x16x32_f16 v[66:69], v[208:211], v[26:29], v[114:117]
	v_mfma_f32_16x16x32_f16 v[78:81], v[212:215], v[30:33], v[66:69]
	v_mfma_f32_16x16x32_f16 v[66:69], v[2:5], v[216:219], v[110:113]
	v_mfma_f32_16x16x32_f16 v[70:73], v[208:211], v[216:219], v[106:109]
	v_mfma_f32_16x16x32_f16 v[66:69], v[6:9], v[224:227], v[66:69]
	v_mfma_f32_16x16x32_f16 v[70:73], v[212:215], v[224:227], v[70:73]
.Lg2p_skip13:
	s_barrier
	ds_read_b128 v[228:231], v135
	ds_read_b128 v[232:235], v135 offset:1024
	ds_read_b128 v[236:239], v135 offset:2048
	ds_read_b128 v[240:243], v135 offset:3072
	s_waitcnt vmcnt(0)
	s_barrier
	s_waitcnt lgkmcnt(0)
	s_bitcmp1_b32 s100, 0
	s_cbranch_scc1 .Lg2p_skip14
	v_mfma_f32_16x16x32_f16 v[94:97], v[228:231], v[10:13], v[94:97]
	v_mfma_f32_16x16x32_f16 v[10:13], v[236:239], v[10:13], v[168:171]
	v_mfma_f32_16x16x32_f16 v[126:129], v[240:243], v[14:17], v[10:13]
	v_mfma_f32_16x16x32_f16 v[10:13], v[228:231], v[18:21], v[172:175]
	v_mfma_f32_16x16x32_f16 v[114:117], v[232:235], v[22:25], v[10:13]
	v_mfma_f32_16x16x32_f16 v[10:13], v[236:239], v[18:21], v[176:179]
	v_mfma_f32_16x16x32_f16 v[118:121], v[240:243], v[22:25], v[10:13]
	v_mfma_f32_16x16x32_f16 v[10:13], v[228:231], v[26:29], v[184:187]
	v_mfma_f32_16x16x32_f16 v[106:109], v[232:235], v[30:33], v[10:13]
	v_mfma_f32_16x16x32_f16 v[10:13], v[236:239], v[26:29], v[188:191]
	v_mfma_f32_16x16x32_f16 v[110:113], v[240:243], v[30:33], v[10:13]
	v_mfma_f32_16x16x32_f16 v[10:13], v[228:231], v[216:219], v[192:195]
	v_mfma_f32_16x16x32_f16 v[122:125], v[232:235], v[14:17], v[94:97]
	v_mfma_f32_16x16x32_f16 v[94:97], v[232:235], v[224:227], v[10:13]
	v_mfma_f32_16x16x32_f16 v[10:13], v[236:239], v[216:219], v[196:199]
	v_mfma_f32_16x16x32_f16 v[102:105], v[240:243], v[224:227], v[10:13]
.Lg2p_skip14:
	s_barrier
	ds_read_b128 v[168:171], v134 offset:49152
	ds_read_b128 v[134:137], v134 offset:50176
	ds_read_b128 v[172:175], v133 offset:49152
	ds_read_b128 v[176:179], v133 offset:50176
	ds_read_b128 v[184:187], v131 offset:49152
	ds_read_b128 v[188:191], v131 offset:50176
	ds_read_b128 v[192:195], v130 offset:49152
	ds_read_b128 v[196:199], v130 offset:50176
	s_barrier
	s_waitcnt lgkmcnt(0)
	s_bitcmp1_b32 s100, 1
	s_cbranch_scc1 .Lg2p_skip15
	v_mfma_f32_16x16x32_f16 v[10:13], v[2:5], v[168:171], v[62:65]
	v_mfma_f32_16x16x32_f16 v[26:29], v[6:9], v[134:137], v[10:13]
	v_mfma_f32_16x16x32_f16 v[10:13], v[208:211], v[168:171], v[58:61]
	v_mfma_f32_16x16x32_f16 v[30:33], v[212:215], v[134:137], v[10:13]
	v_mfma_f32_16x16x32_f16 v[10:13], v[2:5], v[172:175], v[54:57]
	v_mfma_f32_16x16x32_f16 v[18:21], v[6:9], v[176:179], v[10:13]
	v_mfma_f32_16x16x32_f16 v[10:13], v[208:211], v[172:175], v[50:53]
	v_mfma_f32_16x16x32_f16 v[22:25], v[212:215], v[176:179], v[10:13]
	v_mfma_f32_16x16x32_f16 v[10:13], v[2:5], v[184:187], v[46:49]
	v_mfma_f32_16x16x32_f16 v[2:5], v[2:5], v[192:195], v[38:41]
	v_mfma_f32_16x16x32_f16 v[10:13], v[6:9], v[188:191], v[10:13]
	v_mfma_f32_16x16x32_f16 v[14:17], v[208:211], v[184:187], v[42:45]
	v_mfma_f32_16x16x32_f16 v[2:5], v[6:9], v[196:199], v[2:5]
	v_mfma_f32_16x16x32_f16 v[6:9], v[208:211], v[192:195], v[138:141]
	v_mfma_f32_16x16x32_f16 v[14:17], v[212:215], v[188:191], v[14:17]
	v_mfma_f32_16x16x32_f16 v[6:9], v[212:215], v[196:199], v[6:9]
.Lg2p_skip15:
	s_bitcmp1_b32 s100, 1
	s_cbranch_scc1 .Lg2p_skip16
	v_mfma_f32_16x16x32_f16 v[34:37], v[228:231], v[168:171], v[34:37]
	v_mfma_f32_16x16x32_f16 v[58:61], v[232:235], v[134:137], v[34:37]
	v_mfma_f32_16x16x32_f16 v[34:37], v[236:239], v[168:171], v[142:145]
	v_mfma_f32_16x16x32_f16 v[62:65], v[240:243], v[134:137], v[34:37]
	v_mfma_f32_16x16x32_f16 v[34:37], v[228:231], v[172:175], v[154:157]
	v_mfma_f32_16x16x32_f16 v[50:53], v[232:235], v[176:179], v[34:37]
	v_mfma_f32_16x16x32_f16 v[34:37], v[236:239], v[172:175], v[158:161]
	v_mfma_f32_16x16x32_f16 v[54:57], v[240:243], v[176:179], v[34:37]
	v_mfma_f32_16x16x32_f16 v[34:37], v[228:231], v[184:187], v[164:167]
	v_mfma_f32_16x16x32_f16 v[42:45], v[232:235], v[188:191], v[34:37]
	v_mfma_f32_16x16x32_f16 v[34:37], v[236:239], v[184:187], v[220:223]
	v_mfma_f32_16x16x32_f16 v[46:49], v[240:243], v[188:191], v[34:37]
	v_mfma_f32_16x16x32_f16 v[34:37], v[228:231], v[192:195], v[204:207]
	v_mfma_f32_16x16x32_f16 v[38:41], v[236:239], v[192:195], v[200:203]
	v_mfma_f32_16x16x32_f16 v[34:37], v[232:235], v[196:199], v[34:37]
	v_mfma_f32_16x16x32_f16 v[38:41], v[240:243], v[196:199], v[38:41]
